# v8: v7 + DPP wave reductions (no residual prefetch)
# speedup vs baseline: 1.0299x; 1.0021x over previous
; __device__ __forceinline__ float rstd_from_fix(u64_t q) { return __builtin_amdgcn_rsqf((float)q * (1.0f / 16777216.0f) * (1.0f / D) + EPS); }
; __device__ __forceinline__ void unpack8(const u32x4& w, f32x4& a, f32x4& b) { a = (f32x4){bf_lo(w.x), bf_hi(w.x), bf_lo(w.y), bf_hi(w.y)}; b = (f32x4){bf_lo(w.z), bf_hi(w.z), bf_lo(w.w), bf_hi(w.w)}; }
; #define Q4(V) (((unsigned)(int)__builtin_rintf(V[0] * inv) & 255u) | (((unsigned)(int)__builtin_rintf(V[1] * inv) & 255u) << 8) | (((unsigned)(int)__builtin_rintf(V[2] * inv) & 255u) << 16) | (((unsigned)(int)__builtin_rintf(V[3] * inv) & 255u) << 24))
; #define Q4(V) (((unsigned)(int)__builtin_rintf(V[0] * inv) & 255u) | (((unsigned)(int)__builtin_rintf(V[1] * inv) & 255u) << 8) | (((unsigned)(int)__builtin_rintf(V[2] * inv) & 255u) << 16) | (((unsigned)(int)__builtin_rintf(V[3] * inv) & 255u) << 24))
; #define Q4(V) (((unsigned)(int)__builtin_rintf(V[0] * inv) & 255u) | (((unsigned)(int)__builtin_rintf(V[1] * inv) & 255u) << 8) | (((unsigned)(int)__builtin_rintf(V[2] * inv) & 255u) << 16) | (((unsigned)(int)__builtin_rintf(V[3] * inv) & 255u) << 24))
; __device__ __forceinline__ void quant_pass(const bf16_t* XB, unsigned char* XQ, float* rsq, const u64_t* ssq, int gw, int NGW, int lane, bool dry) {
;     ...
;         for (int k = 0; k < 4; ++k) { const int row = r0 + k * NGW; if (row >= NTOK) continue;
;             f32x4 v[4]; unpack8(w0[k], v[0], v[1]); unpack8(w1[k], v[2], v[3]);
;             float am = 0.f;
; #pragma unroll
;             for (int i = 0; i < 4; ++i)
; #pragma unroll
;                 for (int j = 0; j < 4; ++j) am = fmaxf(am, fabsf(v[i][j]));
; #pragma unroll
;             for (int o = 1; o < 64; o <<= 1) am = fmaxf(am, __shfl_xor(am, o));
;             const float sc = am > 0.f ? am * (1.0f / 127.0f) : 1.0f, inv = 1.0f / sc; u32x4 q;
;     ...
;             q.x = Q4(v[0]); q.y = Q4(v[1]); q.z = Q4(v[2]); q.w = Q4(v[3]);
;     ...
;             if (!dry) { ((u32x4*)(XQ + (size_t)row * D))[lane] = q; if (lane == 0) rsq[row] = sc * rstd_from_fix(sq[k]); } }
.LBB0_290:
	s_waitcnt vmcnt(0)
	v_lshlrev_b32_e32 v16, 16, v12
	v_and_b32_e32 v12, 0xffff0000, v12
	v_lshlrev_b32_e32 v17, 16, v13
	v_and_b32_e32 v13, 0xffff0000, v13
	v_lshlrev_b32_e32 v20, 16, v8
	v_and_b32_e32 v21, 0xffff0000, v8
	v_max3_f32 v8, |v16|, 0, |v12|
	v_lshlrev_b32_e32 v18, 16, v14
	v_and_b32_e32 v14, 0xffff0000, v14
	v_max3_f32 v8, v8, |v17|, |v13|
	v_lshlrev_b32_e32 v19, 16, v15
	v_and_b32_e32 v15, 0xffff0000, v15
	v_max3_f32 v8, v8, |v18|, |v14|
	v_max3_f32 v8, v8, |v19|, |v15|
	v_lshlrev_b32_e32 v22, 16, v9
	v_and_b32_e32 v9, 0xffff0000, v9
	v_max3_f32 v8, v8, |v20|, |v21|
	v_lshlrev_b32_e32 v23, 16, v10
	v_and_b32_e32 v32, 0xffff0000, v10
	v_max3_f32 v8, v8, |v22|, |v9|
	v_lshlrev_b32_e32 v33, 16, v11
	v_and_b32_e32 v34, 0xffff0000, v11
	v_max3_f32 v8, v8, |v23|, |v32|
	v_max3_f32 v8, v8, |v33|, |v34|
	s_waitcnt lgkmcnt(0)
	s_mov_b32 s1, 0x40c0c00
	s_ashr_i32 s7, s6, 31
	s_nop 1
	v_max_f32_dpp v10, v8, v8 quad_perm:[1,0,3,2] row_mask:0xf bank_mask:0xf
	s_nop 1
	v_max_f32_dpp v8, v10, v10 quad_perm:[2,3,0,1] row_mask:0xf bank_mask:0xf
	s_nop 1
	v_max_f32_dpp v10, v8, v8 row_half_mirror row_mask:0xf bank_mask:0xf
	s_nop 1
	v_max_f32_dpp v8, v10, v10 row_mirror row_mask:0xf bank_mask:0xf
	v_mov_b32_e32 v10, v8
	s_nop 1
	v_permlane16_swap_b32_e32 v8, v10
	v_max_f32_e32 v8, v8, v10
	v_mov_b32_e32 v10, v8
	s_nop 1
	v_permlane32_swap_b32_e32 v8, v10
	v_max_f32_e32 v8, v8, v10
	s_waitcnt lgkmcnt(0)
	v_mul_f32_e32 v10, 0x3c010204, v8
	v_cmp_lt_f32_e32 vcc, 0, v8
	s_nop 1
	v_cndmask_b32_e32 v8, 1.0, v10, vcc
	v_div_scale_f32 v10, s[8:9], v8, v8, 1.0
	v_rcp_f32_e32 v11, v10
	v_div_scale_f32 v35, vcc, 1.0, v8, 1.0
	s_lshl_b64 s[8:9], s[6:7], 10
	v_fma_f32 v42, -v10, v11, 1.0
	v_fmac_f32_e32 v11, v42, v11
	v_mul_f32_e32 v42, v35, v11
	v_fma_f32 v43, -v10, v42, v35
	v_fmac_f32_e32 v42, v43, v11
	v_fma_f32 v10, -v10, v42, v35
	v_div_fmas_f32 v10, v10, v11, v42
	v_div_fixup_f32 v35, v10, v8, 1.0
	v_mul_f32_e32 v11, v35, v12
	v_mul_f32_e32 v10, v35, v16
	v_mul_f32_e32 v12, v35, v17
	v_mul_f32_e32 v13, v35, v13
	v_rndne_f32_e32 v11, v11
	v_rndne_f32_e32 v10, v10
	v_rndne_f32_e32 v12, v12
	v_rndne_f32_e32 v13, v13
	v_cvt_i32_f32_e32 v11, v11
	v_cvt_i32_f32_sdwa v12, v12 dst_sel:WORD_1 dst_unused:UNUSED_PAD src0_sel:DWORD
	v_cvt_i32_f32_e32 v10, v10
	v_cvt_i32_f32_e32 v13, v13
	v_lshlrev_b32_e32 v11, 8, v11
	v_and_b32_e32 v12, 0xff0000, v12
	v_and_b32_e32 v11, 0xff00, v11
	v_perm_b32 v10, v13, v10, s1
	v_or3_b32 v10, v10, v11, v12
	v_mul_f32_e32 v12, v35, v14
	v_mul_f32_e32 v11, v35, v18
	v_rndne_f32_e32 v12, v12
	v_mul_f32_e32 v13, v35, v19
	v_mul_f32_e32 v14, v35, v15
	v_rndne_f32_e32 v11, v11
	v_cvt_i32_f32_e32 v12, v12
	v_rndne_f32_e32 v13, v13
	v_rndne_f32_e32 v14, v14
	v_cvt_i32_f32_e32 v11, v11
	v_cvt_i32_f32_sdwa v13, v13 dst_sel:WORD_1 dst_unused:UNUSED_PAD src0_sel:DWORD
	v_cvt_i32_f32_e32 v14, v14
	v_lshlrev_b32_e32 v12, 8, v12
	v_and_b32_e32 v12, 0xff00, v12
	v_and_b32_e32 v13, 0xff0000, v13
	v_perm_b32 v11, v14, v11, s1
	v_or3_b32 v11, v11, v12, v13
	v_mul_f32_e32 v13, v35, v21
	v_mul_f32_e32 v12, v35, v20
	v_rndne_f32_e32 v13, v13
	v_mul_f32_e32 v14, v35, v22
	v_mul_f32_e32 v9, v35, v9
	v_rndne_f32_e32 v12, v12
	v_cvt_i32_f32_e32 v13, v13
	v_rndne_f32_e32 v14, v14
	v_rndne_f32_e32 v9, v9
	v_cvt_i32_f32_e32 v12, v12
	v_cvt_i32_f32_sdwa v14, v14 dst_sel:WORD_1 dst_unused:UNUSED_PAD src0_sel:DWORD
	v_cvt_i32_f32_e32 v9, v9
	v_lshlrev_b32_e32 v13, 8, v13
	v_and_b32_e32 v13, 0xff00, v13
	v_and_b32_e32 v14, 0xff0000, v14
	v_perm_b32 v9, v9, v12, s1
	v_or3_b32 v12, v9, v13, v14
	v_mul_f32_e32 v13, v35, v32
	v_mul_f32_e32 v9, v35, v23
	v_rndne_f32_e32 v13, v13
	v_mul_f32_e32 v14, v35, v33
	v_mul_f32_e32 v15, v35, v34
	v_rndne_f32_e32 v9, v9
	v_cvt_i32_f32_e32 v13, v13
	v_rndne_f32_e32 v14, v14
	v_rndne_f32_e32 v15, v15
	v_cvt_i32_f32_e32 v9, v9
	v_cvt_i32_f32_sdwa v14, v14 dst_sel:WORD_1 dst_unused:UNUSED_PAD src0_sel:DWORD
	v_cvt_i32_f32_e32 v15, v15
	v_lshlrev_b32_e32 v13, 8, v13
	v_and_b32_e32 v13, 0xff00, v13
	v_and_b32_e32 v14, 0xff0000, v14
	v_perm_b32 v9, v15, v9, s1
	v_or3_b32 v13, v9, v13, v14
	v_lshl_add_u64 v[14:15], v[26:27], 0, s[8:9]
	flat_store_dwordx4 v[14:15], v[10:13]
	s_and_saveexec_b64 s[8:9], s[2:3]
	s_cbranch_execz .LBB0_292
	v_ffbh_u32_e32 v9, v31
	v_min_u32_e32 v9, 32, v9
	v_lshlrev_b64 v[10:11], v9, v[30:31]
	v_min_u32_e32 v10, 1, v10
	v_or_b32_e32 v10, v11, v10
	v_cvt_f32_u32_e32 v10, v10
	v_sub_u32_e32 v9, 32, v9
	s_lshl_b64 s[6:7], s[6:7], 2
	s_add_u32 s6, s16, s6
	v_ldexp_f32 v9, v10, v9
	v_mul_f32_e32 v9, 0x33800000, v9
	v_fmamk_f32 v9, v9, 0x3a800000, v249
	v_rsq_f32_e32 v9, v9
	s_addc_u32 s7, s17, s7
	v_mul_f32_e32 v10, v9, v8
	v_mov_b64_e32 v[8:9], s[6:7]
	flat_store_dword v[8:9], v10

; __device__ __forceinline__ float rstd_from_fix(u64_t q) { return __builtin_amdgcn_rsqf((float)q * (1.0f / 16777216.0f) * (1.0f / D) + EPS); }
; __device__ __forceinline__ void unpack8(const u32x4& w, f32x4& a, f32x4& b) { a = (f32x4){bf_lo(w.x), bf_hi(w.x), bf_lo(w.y), bf_hi(w.y)}; b = (f32x4){bf_lo(w.z), bf_hi(w.z), bf_lo(w.w), bf_hi(w.w)}; }
; #define Q4(V) (((unsigned)(int)__builtin_rintf(V[0] * inv) & 255u) | (((unsigned)(int)__builtin_rintf(V[1] * inv) & 255u) << 8) | (((unsigned)(int)__builtin_rintf(V[2] * inv) & 255u) << 16) | (((unsigned)(int)__builtin_rintf(V[3] * inv) & 255u) << 24))
; #define Q4(V) (((unsigned)(int)__builtin_rintf(V[0] * inv) & 255u) | (((unsigned)(int)__builtin_rintf(V[1] * inv) & 255u) << 8) | (((unsigned)(int)__builtin_rintf(V[2] * inv) & 255u) << 16) | (((unsigned)(int)__builtin_rintf(V[3] * inv) & 255u) << 24))
; #define Q4(V) (((unsigned)(int)__builtin_rintf(V[0] * inv) & 255u) | (((unsigned)(int)__builtin_rintf(V[1] * inv) & 255u) << 8) | (((unsigned)(int)__builtin_rintf(V[2] * inv) & 255u) << 16) | (((unsigned)(int)__builtin_rintf(V[3] * inv) & 255u) << 24))
; __device__ __forceinline__ void quant_pass(const bf16_t* XB, unsigned char* XQ, float* rsq, const u64_t* ssq, int gw, int NGW, int lane, bool dry) {
;     ...
;         for (int k = 0; k < 4; ++k) { const int row = r0 + k * NGW; if (row >= NTOK) continue;
;             f32x4 v[4]; unpack8(w0[k], v[0], v[1]); unpack8(w1[k], v[2], v[3]);
;             float am = 0.f;
; #pragma unroll
;             for (int i = 0; i < 4; ++i)
; #pragma unroll
;                 for (int j = 0; j < 4; ++j) am = fmaxf(am, fabsf(v[i][j]));
; #pragma unroll
;             for (int o = 1; o < 64; o <<= 1) am = fmaxf(am, __shfl_xor(am, o));
;             const float sc = am > 0.f ? am * (1.0f / 127.0f) : 1.0f, inv = 1.0f / sc; u32x4 q;
;     ...
;             q.x = Q4(v[0]); q.y = Q4(v[1]); q.z = Q4(v[2]); q.w = Q4(v[3]);
;     ...
;             if (!dry) { ((u32x4*)(XQ + (size_t)row * D))[lane] = q; if (lane == 0) rsq[row] = sc * rstd_from_fix(sq[k]); } }
.LBB0_294:
	s_waitcnt vmcnt(0)
	v_lshlrev_b32_e32 v34, 16, v16
	v_and_b32_e32 v35, 0xffff0000, v16
	v_lshlrev_b32_e32 v42, 16, v17
	v_and_b32_e32 v17, 0xffff0000, v17
	v_max3_f32 v16, |v34|, 0, |v35|
	v_lshlrev_b32_e32 v43, 16, v18
	v_and_b32_e32 v44, 0xffff0000, v18
	v_max3_f32 v16, v16, |v42|, |v17|
	v_lshlrev_b32_e32 v45, 16, v19
	v_and_b32_e32 v19, 0xffff0000, v19
	v_max3_f32 v16, v16, |v43|, |v44|
	v_lshlrev_b32_e32 v46, 16, v20
	v_and_b32_e32 v20, 0xffff0000, v20
	v_max3_f32 v16, v16, |v45|, |v19|
	v_lshlrev_b32_e32 v47, 16, v21
	v_and_b32_e32 v21, 0xffff0000, v21
	v_max3_f32 v16, v16, |v46|, |v20|
	v_lshlrev_b32_e32 v48, 16, v22
	v_and_b32_e32 v22, 0xffff0000, v22
	v_max3_f32 v16, v16, |v47|, |v21|
	v_lshlrev_b32_e32 v49, 16, v23
	v_and_b32_e32 v23, 0xffff0000, v23
	v_max3_f32 v16, v16, |v48|, |v22|
	v_max3_f32 v16, v16, |v49|, |v23|
	s_waitcnt lgkmcnt(0)
	s_nop 1
	v_max_f32_dpp v18, v16, v16 quad_perm:[1,0,3,2] row_mask:0xf bank_mask:0xf
	s_nop 1
	v_max_f32_dpp v16, v18, v18 quad_perm:[2,3,0,1] row_mask:0xf bank_mask:0xf
	s_nop 1
	v_max_f32_dpp v18, v16, v16 row_half_mirror row_mask:0xf bank_mask:0xf
	s_nop 1
	v_max_f32_dpp v16, v18, v18 row_mirror row_mask:0xf bank_mask:0xf
	v_mov_b32_e32 v18, v16
	s_nop 1
	v_permlane16_swap_b32_e32 v16, v18
	v_max_f32_e32 v16, v16, v18
	v_mov_b32_e32 v18, v16
	s_nop 1
	v_permlane32_swap_b32_e32 v16, v18
	v_max_f32_e32 v16, v16, v18
	s_waitcnt lgkmcnt(0)
	v_mul_f32_e32 v18, 0x3c010204, v16
	v_cmp_lt_f32_e32 vcc, 0, v16
	s_nop 1
	v_cndmask_b32_e32 v16, 1.0, v18, vcc
	v_div_scale_f32 v18, s[8:9], v16, v16, 1.0
	v_rcp_f32_e32 v50, v18
	v_div_scale_f32 v51, vcc, 1.0, v16, 1.0
	v_fma_f32 v52, -v18, v50, 1.0
	v_fmac_f32_e32 v50, v52, v50
	v_mul_f32_e32 v52, v51, v50
	v_fma_f32 v53, -v18, v52, v51
	v_fmac_f32_e32 v52, v53, v50
	v_fma_f32 v18, -v18, v52, v51
	v_div_fmas_f32 v18, v18, v50, v52
	v_div_fixup_f32 v50, v18, v16, 1.0
	v_mul_f32_e32 v18, v50, v34
	v_mul_f32_e32 v34, v50, v35
	v_mul_f32_e32 v35, v50, v42
	v_mul_f32_e32 v17, v50, v17
	v_rndne_f32_e32 v34, v34
	v_rndne_f32_e32 v18, v18
	v_rndne_f32_e32 v35, v35
	v_rndne_f32_e32 v17, v17
	v_cvt_i32_f32_e32 v34, v34
	v_cvt_i32_f32_sdwa v35, v35 dst_sel:WORD_1 dst_unused:UNUSED_PAD src0_sel:DWORD
	v_cvt_i32_f32_e32 v18, v18
	v_cvt_i32_f32_e32 v17, v17
	v_lshlrev_b32_e32 v34, 8, v34
	v_and_b32_e32 v35, 0xff0000, v35
	v_and_b32_e32 v34, 0xff00, v34
	v_perm_b32 v17, v17, v18, s1
	v_or3_b32 v18, v17, v34, v35
	v_mul_f32_e32 v34, v50, v44
	v_mul_f32_e32 v17, v50, v43
	v_rndne_f32_e32 v34, v34
	v_mul_f32_e32 v35, v50, v45
	v_mul_f32_e32 v19, v50, v19
	v_rndne_f32_e32 v17, v17
	v_cvt_i32_f32_e32 v34, v34
	v_rndne_f32_e32 v35, v35
	v_rndne_f32_e32 v19, v19
	v_cvt_i32_f32_e32 v17, v17
	v_cvt_i32_f32_sdwa v35, v35 dst_sel:WORD_1 dst_unused:UNUSED_PAD src0_sel:DWORD
	v_cvt_i32_f32_e32 v19, v19
	v_lshlrev_b32_e32 v34, 8, v34
	v_and_b32_e32 v34, 0xff00, v34
	v_and_b32_e32 v35, 0xff0000, v35
	v_perm_b32 v17, v19, v17, s1
	v_mul_f32_e32 v20, v50, v20
	v_or3_b32 v19, v17, v34, v35
	v_mul_f32_e32 v17, v50, v46
	v_rndne_f32_e32 v20, v20
	v_mul_f32_e32 v34, v50, v47
	v_mul_f32_e32 v21, v50, v21
	v_rndne_f32_e32 v17, v17
	v_cvt_i32_f32_e32 v20, v20
	v_rndne_f32_e32 v34, v34
	v_rndne_f32_e32 v21, v21
	v_cvt_i32_f32_e32 v17, v17
	v_cvt_i32_f32_sdwa v34, v34 dst_sel:WORD_1 dst_unused:UNUSED_PAD src0_sel:DWORD
	v_cvt_i32_f32_e32 v21, v21
	v_lshlrev_b32_e32 v20, 8, v20
	v_and_b32_e32 v20, 0xff00, v20
	v_and_b32_e32 v34, 0xff0000, v34
	v_perm_b32 v17, v21, v17, s1
	v_or3_b32 v20, v17, v20, v34
	v_mul_f32_e32 v17, v50, v48
	v_mul_f32_e32 v21, v50, v22
	v_mul_f32_e32 v23, v50, v23
	v_rndne_f32_e32 v17, v17
	v_rndne_f32_e32 v21, v21
	v_mul_f32_e32 v22, v50, v49
	v_rndne_f32_e32 v23, v23
	v_cvt_i32_f32_e32 v17, v17
	v_cvt_i32_f32_e32 v21, v21
	v_rndne_f32_e32 v22, v22
	v_cvt_i32_f32_e32 v23, v23
	v_cvt_i32_f32_sdwa v22, v22 dst_sel:WORD_1 dst_unused:UNUSED_PAD src0_sel:DWORD
	v_lshlrev_b32_e32 v21, 8, v21
	v_and_b32_e32 v21, 0xff00, v21
	v_perm_b32 v17, v23, v17, s1
	s_ashr_i32 s1, s0, 31
	v_and_b32_e32 v22, 0xff0000, v22
	s_lshl_b64 s[8:9], s[0:1], 10
	v_or3_b32 v21, v17, v21, v22
	v_lshl_add_u64 v[22:23], v[26:27], 0, s[8:9]
	flat_store_dwordx4 v[22:23], v[18:21]
	s_and_saveexec_b64 s[8:9], s[2:3]
	s_cbranch_execz .LBB0_296
	v_ffbh_u32_e32 v17, v33
	v_min_u32_e32 v17, 32, v17
	v_lshlrev_b64 v[18:19], v17, v[32:33]
	v_min_u32_e32 v18, 1, v18
	v_or_b32_e32 v18, v19, v18
	v_cvt_f32_u32_e32 v18, v18
	v_sub_u32_e32 v17, 32, v17
	s_lshl_b64 s[10:11], s[0:1], 2
	s_add_u32 s10, s16, s10
	v_ldexp_f32 v17, v18, v17
	v_mul_f32_e32 v17, 0x33800000, v17
	v_fmamk_f32 v17, v17, 0x3a800000, v249
	v_rsq_f32_e32 v17, v17
	s_addc_u32 s11, s17, s11
	v_mul_f32_e32 v18, v17, v16
	v_mov_b64_e32 v[16:17], s[10:11]
	flat_store_dword v[16:17], v18

; __device__ __forceinline__ float rstd_from_fix(u64_t q) { return __builtin_amdgcn_rsqf((float)q * (1.0f / 16777216.0f) * (1.0f / D) + EPS); }
; __device__ __forceinline__ void unpack8(const u32x4& w, f32x4& a, f32x4& b) { a = (f32x4){bf_lo(w.x), bf_hi(w.x), bf_lo(w.y), bf_hi(w.y)}; b = (f32x4){bf_lo(w.z), bf_hi(w.z), bf_lo(w.w), bf_hi(w.w)}; }
; #define Q4(V) (((unsigned)(int)__builtin_rintf(V[0] * inv) & 255u) | (((unsigned)(int)__builtin_rintf(V[1] * inv) & 255u) << 8) | (((unsigned)(int)__builtin_rintf(V[2] * inv) & 255u) << 16) | (((unsigned)(int)__builtin_rintf(V[3] * inv) & 255u) << 24))
; #define Q4(V) (((unsigned)(int)__builtin_rintf(V[0] * inv) & 255u) | (((unsigned)(int)__builtin_rintf(V[1] * inv) & 255u) << 8) | (((unsigned)(int)__builtin_rintf(V[2] * inv) & 255u) << 16) | (((unsigned)(int)__builtin_rintf(V[3] * inv) & 255u) << 24))
; #define Q4(V) (((unsigned)(int)__builtin_rintf(V[0] * inv) & 255u) | (((unsigned)(int)__builtin_rintf(V[1] * inv) & 255u) << 8) | (((unsigned)(int)__builtin_rintf(V[2] * inv) & 255u) << 16) | (((unsigned)(int)__builtin_rintf(V[3] * inv) & 255u) << 24))
; __device__ __forceinline__ void quant_pass(const bf16_t* XB, unsigned char* XQ, float* rsq, const u64_t* ssq, int gw, int NGW, int lane, bool dry) {
;     ...
;         for (int k = 0; k < 4; ++k) { const int row = r0 + k * NGW; if (row >= NTOK) continue;
;             f32x4 v[4]; unpack8(w0[k], v[0], v[1]); unpack8(w1[k], v[2], v[3]);
;             float am = 0.f;
; #pragma unroll
;             for (int i = 0; i < 4; ++i)
; #pragma unroll
;                 for (int j = 0; j < 4; ++j) am = fmaxf(am, fabsf(v[i][j]));
; #pragma unroll
;             for (int o = 1; o < 64; o <<= 1) am = fmaxf(am, __shfl_xor(am, o));
;             const float sc = am > 0.f ? am * (1.0f / 127.0f) : 1.0f, inv = 1.0f / sc; u32x4 q;
;     ...
;             q.x = Q4(v[0]); q.y = Q4(v[1]); q.z = Q4(v[2]); q.w = Q4(v[3]);
;     ...
;             if (!dry) { ((u32x4*)(XQ + (size_t)row * D))[lane] = q; if (lane == 0) rsq[row] = sc * rstd_from_fix(sq[k]); } }
.LBB0_298:
	s_waitcnt vmcnt(0)
	v_lshlrev_b32_e32 v8, 16, v0
	v_and_b32_e32 v9, 0xffff0000, v0
	v_lshlrev_b32_e32 v10, 16, v1
	v_and_b32_e32 v1, 0xffff0000, v1
	v_max3_f32 v0, |v8|, 0, |v9|
	v_lshlrev_b32_e32 v11, 16, v2
	v_and_b32_e32 v12, 0xffff0000, v2
	v_max3_f32 v0, v0, |v10|, |v1|
	v_lshlrev_b32_e32 v13, 16, v3
	v_and_b32_e32 v3, 0xffff0000, v3
	v_max3_f32 v0, v0, |v11|, |v12|
	s_waitcnt lgkmcnt(0)
	v_lshlrev_b32_e32 v14, 16, v4
	v_and_b32_e32 v4, 0xffff0000, v4
	v_max3_f32 v0, v0, |v13|, |v3|
	v_lshlrev_b32_e32 v15, 16, v5
	v_and_b32_e32 v5, 0xffff0000, v5
	v_max3_f32 v0, v0, |v14|, |v4|
	v_lshlrev_b32_e32 v16, 16, v6
	v_and_b32_e32 v6, 0xffff0000, v6
	v_max3_f32 v0, v0, |v15|, |v5|
	v_lshlrev_b32_e32 v17, 16, v7
	v_and_b32_e32 v7, 0xffff0000, v7
	v_max3_f32 v0, v0, |v16|, |v6|
	v_max3_f32 v0, v0, |v17|, |v7|
	s_waitcnt lgkmcnt(0)
	s_mov_b32 s1, 0x40c0c00
	s_ashr_i32 s5, s4, 31
	s_nop 1
	v_max_f32_dpp v2, v0, v0 quad_perm:[1,0,3,2] row_mask:0xf bank_mask:0xf
	s_nop 1
	v_max_f32_dpp v0, v2, v2 quad_perm:[2,3,0,1] row_mask:0xf bank_mask:0xf
	s_nop 1
	v_max_f32_dpp v2, v0, v0 row_half_mirror row_mask:0xf bank_mask:0xf
	s_nop 1
	v_max_f32_dpp v0, v2, v2 row_mirror row_mask:0xf bank_mask:0xf
	v_mov_b32_e32 v2, v0
	s_nop 1
	v_permlane16_swap_b32_e32 v0, v2
	v_max_f32_e32 v0, v0, v2
	v_mov_b32_e32 v2, v0
	s_nop 1
	v_permlane32_swap_b32_e32 v0, v2
	v_max_f32_e32 v0, v0, v2
	s_waitcnt lgkmcnt(0)
	v_mul_f32_e32 v2, 0x3c010204, v0
	v_cmp_lt_f32_e32 vcc, 0, v0
	s_nop 1
	v_cndmask_b32_e32 v0, 1.0, v2, vcc
	v_div_scale_f32 v2, s[6:7], v0, v0, 1.0
	v_rcp_f32_e32 v18, v2
	v_div_scale_f32 v19, vcc, 1.0, v0, 1.0
	s_lshl_b64 s[6:7], s[4:5], 10
	v_fma_f32 v20, -v2, v18, 1.0
	v_fmac_f32_e32 v18, v20, v18
	v_mul_f32_e32 v20, v19, v18
	v_fma_f32 v21, -v2, v20, v19
	v_fmac_f32_e32 v20, v21, v18
	v_fma_f32 v2, -v2, v20, v19
	v_div_fmas_f32 v2, v2, v18, v20
	v_div_fixup_f32 v18, v2, v0, 1.0
	v_mul_f32_e32 v2, v18, v8
	v_mul_f32_e32 v8, v18, v9
	v_mul_f32_e32 v9, v18, v10
	v_mul_f32_e32 v1, v18, v1
	v_rndne_f32_e32 v8, v8
	v_rndne_f32_e32 v2, v2
	v_rndne_f32_e32 v9, v9
	v_rndne_f32_e32 v1, v1
	v_cvt_i32_f32_e32 v8, v8
	v_cvt_i32_f32_sdwa v9, v9 dst_sel:WORD_1 dst_unused:UNUSED_PAD src0_sel:DWORD
	v_cvt_i32_f32_e32 v2, v2
	v_cvt_i32_f32_e32 v1, v1
	v_lshlrev_b32_e32 v8, 8, v8
	v_and_b32_e32 v9, 0xff0000, v9
	v_and_b32_e32 v8, 0xff00, v8
	v_perm_b32 v1, v1, v2, s1
	v_or3_b32 v2, v1, v8, v9
	v_mul_f32_e32 v8, v18, v12
	v_mul_f32_e32 v1, v18, v11
	v_rndne_f32_e32 v8, v8
	v_mul_f32_e32 v9, v18, v13
	v_mul_f32_e32 v3, v18, v3
	v_rndne_f32_e32 v1, v1
	v_cvt_i32_f32_e32 v8, v8
	v_rndne_f32_e32 v9, v9
	v_rndne_f32_e32 v3, v3
	v_cvt_i32_f32_e32 v1, v1
	v_cvt_i32_f32_sdwa v9, v9 dst_sel:WORD_1 dst_unused:UNUSED_PAD src0_sel:DWORD
	v_cvt_i32_f32_e32 v3, v3
	v_lshlrev_b32_e32 v8, 8, v8
	v_and_b32_e32 v8, 0xff00, v8
	v_and_b32_e32 v9, 0xff0000, v9
	v_perm_b32 v1, v3, v1, s1
	v_mul_f32_e32 v4, v18, v4
	v_or3_b32 v3, v1, v8, v9
	v_mul_f32_e32 v1, v18, v14
	v_rndne_f32_e32 v4, v4
	v_mul_f32_e32 v8, v18, v15
	v_mul_f32_e32 v5, v18, v5
	v_rndne_f32_e32 v1, v1
	v_cvt_i32_f32_e32 v4, v4
	v_rndne_f32_e32 v8, v8
	v_rndne_f32_e32 v5, v5
	v_cvt_i32_f32_e32 v1, v1
	v_cvt_i32_f32_sdwa v8, v8 dst_sel:WORD_1 dst_unused:UNUSED_PAD src0_sel:DWORD
	v_cvt_i32_f32_e32 v5, v5
	v_lshlrev_b32_e32 v4, 8, v4
	v_and_b32_e32 v4, 0xff00, v4
	v_and_b32_e32 v8, 0xff0000, v8
	v_perm_b32 v1, v5, v1, s1
	v_mul_f32_e32 v5, v18, v6
	v_or3_b32 v4, v1, v4, v8
	v_mul_f32_e32 v1, v18, v16
	v_rndne_f32_e32 v5, v5
	v_mul_f32_e32 v6, v18, v17
	v_mul_f32_e32 v7, v18, v7
	v_rndne_f32_e32 v1, v1
	v_cvt_i32_f32_e32 v5, v5
	v_rndne_f32_e32 v6, v6
	v_rndne_f32_e32 v7, v7
	v_cvt_i32_f32_e32 v1, v1
	v_cvt_i32_f32_sdwa v6, v6 dst_sel:WORD_1 dst_unused:UNUSED_PAD src0_sel:DWORD
	v_cvt_i32_f32_e32 v7, v7
	v_lshlrev_b32_e32 v5, 8, v5
	v_and_b32_e32 v5, 0xff00, v5
	v_and_b32_e32 v6, 0xff0000, v6
	v_perm_b32 v1, v7, v1, s1
	v_or3_b32 v5, v1, v5, v6
	v_lshl_add_u64 v[6:7], v[26:27], 0, s[6:7]
	flat_store_dwordx4 v[6:7], v[2:5]
	s_and_saveexec_b64 s[6:7], s[2:3]
	s_cbranch_execz .LBB0_285
	v_ffbh_u32_e32 v1, v29
	v_min_u32_e32 v1, 32, v1
	v_lshlrev_b64 v[2:3], v1, v[28:29]
	v_min_u32_e32 v2, 1, v2
	v_or_b32_e32 v2, v3, v2
	v_cvt_f32_u32_e32 v2, v2
	v_sub_u32_e32 v1, 32, v1
	s_lshl_b64 s[4:5], s[4:5], 2
	s_add_u32 s4, s16, s4
	v_ldexp_f32 v1, v2, v1
	v_mul_f32_e32 v1, 0x33800000, v1
	v_fmamk_f32 v1, v1, 0x3a800000, v249
	v_rsq_f32_e32 v1, v1
	s_addc_u32 s5, s17, s5
	v_mul_f32_e32 v2, v1, v0
	v_mov_b64_e32 v[0:1], s[4:5]
	flat_store_dword v[0:1], v2
	s_branch .LBB0_285

; __device__ __forceinline__ unsigned pk_bf16(float lo, float hi) { f32x2 v = {lo, hi}; bf16x2_t b = __builtin_convertvector(v, bf16x2_t); return __builtin_bit_cast(unsigned, b); }
; __device__ __forceinline__ float bf_lo(unsigned w) { return __uint_as_float(w << 16); }
; __device__ __forceinline__ float bf_hi(unsigned w) { return __uint_as_float(w & 0xffff0000u); }
; __device__ __forceinline__ void phase_kxnorm(const Frame& F, const Params& P) {
;     ...
;     for (int it = gw; it < 2 * B * MEM * XH; it += NGW) { const int h = it & 3, row = (it >> 2) & (B * MEM - 1), l = it >> 13;
;         bf16_t* p = (bf16_t*)(F.ws + WS_KXV) + ((size_t)l * B * MEM + row) * 1024 + h * XHD + 2 * lane; const unsigned w = *(const unsigned*)p;
;         const float a = bf_lo(w), b = bf_hi(w); const float ss = wave_sum(a * a + b * b); const float r = __builtin_amdgcn_rsqf(ss * (1.0f / XHD) + EPS); const float* g = P.in[21] + l * XHD + 2 * lane;
;         *(unsigned*)p = pk_bf16(a * r * g[0], b * r * g[1]); }
.LBB0_574:
	s_ashr_i32 s6, s4, 13
	s_ashr_i32 s7, s6, 31
	s_and_b32 s5, s2, 0x1ffc00
	s_lshl_b64 s[8:9], s[6:7], 22
	s_add_u32 s7, s0, s8
	s_addc_u32 s8, s1, s9
	s_lshl_b32 s5, s5, 1
	s_add_u32 s5, s7, s5
	s_addc_u32 s7, s8, 0
	s_and_b32 s8, s3, 0x180
	s_lshl_b32 s8, s8, 1
	s_add_u32 s8, s5, s8
	s_addc_u32 s9, s7, 0
	v_lshl_add_u64 v[8:9], s[8:9], 0, v[112:113]
	flat_load_dword v13, v[8:9]
	s_lshl_b32 s6, s6, 7
	s_ashr_i32 s7, s6, 31
	v_lshl_add_u64 v[10:11], s[6:7], 2, v[0:1]
	global_load_dwordx2 v[10:11], v[10:11], off
	s_add_i32 s4, s4, s76
	s_add_i32 s3, s3, s82
	s_add_i32 s2, s2, s89
	s_cmpk_lt_i32 s4, 0x4000
	s_waitcnt vmcnt(0) lgkmcnt(0)
	v_lshlrev_b32_e32 v12, 16, v13
	v_and_b32_e32 v13, 0xffff0000, v13
	v_pk_mul_f32 v[14:15], v[12:13], v[12:13]
	s_nop 0
	v_add_f32_e32 v14, v14, v15
	s_waitcnt lgkmcnt(0)
	s_nop 1
	v_add_f32_dpp v15, v14, v14 quad_perm:[1,0,3,2] row_mask:0xf bank_mask:0xf
	s_nop 1
	v_add_f32_dpp v14, v15, v15 quad_perm:[2,3,0,1] row_mask:0xf bank_mask:0xf
	s_nop 1
	v_add_f32_dpp v15, v14, v14 row_half_mirror row_mask:0xf bank_mask:0xf
	s_nop 1
	v_add_f32_dpp v14, v15, v15 row_mirror row_mask:0xf bank_mask:0xf
	v_mov_b32_e32 v15, v14
	s_nop 1
	v_permlane16_swap_b32_e32 v14, v15
	v_add_f32_e32 v14, v14, v15
	v_mov_b32_e32 v15, v14
	s_nop 1
	v_permlane32_swap_b32_e32 v14, v15
	v_add_f32_e32 v14, v14, v15
	s_waitcnt lgkmcnt(0)
	v_fmamk_f32 v14, v14, 0x3c000000, v249
	v_rsq_f32_e32 v14, v14
	s_nop 0
	v_pk_mul_f32 v[12:13], v[14:15], v[12:13] op_sel_hi:[0,1]
	v_pk_mul_f32 v[10:11], v[10:11], v[12:13]
	s_nop 0
	v_cvt_pk_bf16_f32 v10, v10, v11
	flat_store_dword v[8:9], v10
	s_cbranch_scc1 .LBB0_574

; __device__ __forceinline__ float rstd_from_fix(u64_t q) { return __builtin_amdgcn_rsqf((float)q * (1.0f / 16777216.0f) * (1.0f / D) + EPS); }
; __device__ __forceinline__ void unpack8(const u32x4& w, f32x4& a, f32x4& b) { a = (f32x4){bf_lo(w.x), bf_hi(w.x), bf_lo(w.y), bf_hi(w.y)}; b = (f32x4){bf_lo(w.z), bf_hi(w.z), bf_lo(w.w), bf_hi(w.w)}; }
; #define Q4(V) (((unsigned)(int)__builtin_rintf(V[0] * inv) & 255u) | (((unsigned)(int)__builtin_rintf(V[1] * inv) & 255u) << 8) | (((unsigned)(int)__builtin_rintf(V[2] * inv) & 255u) << 16) | (((unsigned)(int)__builtin_rintf(V[3] * inv) & 255u) << 24))
; __device__ __forceinline__ void phase_moe_gather(const Frame& F, bool dry) {
;     ...
;     for (int t0 = gw; t0 < NTOK; t0 += 2 * NGW) {
;         u32x4 w0[2], w1[2]; int e[4], rk[4]; u64_t sq[2];
; #pragma unroll
;         for (int k = 0; k < 2; ++k) { const int tok = t0 + k * NGW; const bool ok = tok < NTOK; const int tk = ok ? tok : 0;
;             w0[k] = ((const u32x4*)(XB + (size_t)tk * D))[2 * lane]; w1[k] = ((const u32x4*)(XB + (size_t)tk * D))[2 * lane + 1];
;             e[2 * k] = tope[2 * tk]; e[2 * k + 1] = tope[2 * tk + 1]; rk[2 * k] = tokslot[2 * tk]; rk[2 * k + 1] = tokslot[2 * tk + 1]; sq[k] = ssq[tk]; }
; #pragma unroll
;         for (int k = 0; k < 2; ++k) { const int tok = t0 + k * NGW; if (tok >= NTOK) continue;
;             f32x4 v[4]; unpack8(w0[k], v[0], v[1]); unpack8(w1[k], v[2], v[3]);
;             float am = 0.f;
; #pragma unroll
;             for (int i = 0; i < 4; ++i)
; #pragma unroll
;                 for (int j = 0; j < 4; ++j) am = fmaxf(am, fabsf(v[i][j]));
; #pragma unroll
;             for (int o = 1; o < 64; o <<= 1) am = fmaxf(am, __shfl_xor(am, o));
;             const float sc = am > 0.f ? am * (1.0f / 127.0f) : 1.0f, inv = 1.0f / sc; u32x4 q;
;     ...
;             q.x = Q4(v[0]); q.y = Q4(v[1]); q.z = Q4(v[2]); q.w = Q4(v[3]);
;     ...
;             const float rr = rstd_from_fix(sq[k]);
; #pragma unroll
;             for (int s2 = 0; s2 < 2; ++s2) { const int ee = e[2 * k + s2]; int ps = 0;
; #pragma unroll
;                 for (int j = 0; j < NE; ++j) ps = (ee == j) ? pstart[j] : ps;
;                 const int slot = ps + rk[2 * k + s2];
;                 if (!dry) { ((u32x4*)(XP8 + (size_t)slot * D))[lane] = q; if (lane == 0) { tokslot[2 * tok + s2] = slot; slotr[slot] = sc * rr; } } } }
.LBB0_1457:
	s_add_i32 s10, s8, 1
	s_ashr_i32 s11, s10, 31
	s_ashr_i32 s9, s8, 31
	s_lshl_b64 s[18:19], s[10:11], 2
	s_add_u32 s10, s2, s18
	s_addc_u32 s11, s3, s19
	s_lshl_b64 s[14:15], s[8:9], 2
	v_mov_b64_e32 v[0:1], s[10:11]
	s_add_u32 s10, s36, s14
	s_addc_u32 s11, s37, s15
	s_add_u32 s18, s36, s18
	s_addc_u32 s19, s37, s19
	s_add_i32 s9, s12, s76
	s_cmp_lt_i32 s9, 0x8000
	flat_load_dword v47, v[0:1]
	v_mov_b64_e32 v[0:1], s[18:19]
	s_cselect_b32 s18, s9, 0
	s_ashr_i32 s19, s18, 31
	s_lshl_b64 s[20:21], s[18:19], 11
	flat_load_dword v48, v[0:1]
	v_lshl_add_u64 v[0:1], v[12:13], 0, s[20:21]
	s_lshl_b32 s20, s18, 1
	s_ashr_i32 s21, s20, 31
	s_lshl_b64 s[20:21], s[20:21], 2
	s_add_u32 s22, s2, s20
	s_addc_u32 s23, s3, s21
	s_add_u32 s20, s36, s20
	s_addc_u32 s21, s37, s21
	s_lshl_b64 s[18:19], s[18:19], 3
	v_mov_b64_e32 v[8:9], s[22:23]
	s_add_u32 s18, s16, s18
	flat_load_dwordx4 v[4:7], v[0:1]
	s_nop 0
	flat_load_dwordx4 v[0:3], v[0:1] offset:16
	s_addc_u32 s19, s17, s19
	flat_load_dwordx2 v[16:17], v[8:9]
	v_mov_b64_e32 v[8:9], s[20:21]
	s_ashr_i32 s13, s12, 31
	flat_load_dwordx2 v[18:19], v[8:9]
	v_mov_b64_e32 v[8:9], s[18:19]
	s_lshl_b64 s[18:19], s[12:13], 3
	s_add_u32 s18, s16, s18
	s_addc_u32 s19, s17, s19
	flat_load_dwordx2 v[22:23], v[8:9]
	v_mov_b64_e32 v[8:9], s[18:19]
	s_add_u32 s14, s2, s14
	flat_load_dwordx2 v[24:25], v[8:9]
	v_mov_b64_e32 v[8:9], s[10:11]
	s_addc_u32 s15, s3, s15
	s_lshl_b64 s[12:13], s[12:13], 11
	flat_load_dword v49, v[8:9]
	v_mov_b64_e32 v[8:9], s[14:15]
	v_lshl_add_u64 v[52:53], v[12:13], 0, s[12:13]
	flat_load_dword v50, v[8:9]
	s_nop 0
	flat_load_dwordx4 v[8:11], v[52:53] offset:16
	s_nop 0
	flat_load_dwordx4 v[52:55], v[52:53]
	s_waitcnt vmcnt(0) lgkmcnt(0)
	v_lshlrev_b32_e32 v60, 16, v8
	v_lshlrev_b32_e32 v56, 16, v52
	v_and_b32_e32 v52, 0xffff0000, v52
	v_lshlrev_b32_e32 v57, 16, v53
	v_and_b32_e32 v53, 0xffff0000, v53
	v_and_b32_e32 v61, 0xffff0000, v8
	v_max3_f32 v8, |v56|, 0, |v52|
	v_lshlrev_b32_e32 v58, 16, v54
	v_and_b32_e32 v54, 0xffff0000, v54
	v_max3_f32 v8, v8, |v57|, |v53|
	v_lshlrev_b32_e32 v59, 16, v55
	v_and_b32_e32 v55, 0xffff0000, v55
	v_max3_f32 v8, v8, |v58|, |v54|
	v_max3_f32 v8, v8, |v59|, |v55|
	v_lshlrev_b32_e32 v62, 16, v9
	v_and_b32_e32 v63, 0xffff0000, v9
	v_max3_f32 v8, v8, |v60|, |v61|
	v_lshlrev_b32_e32 v64, 16, v10
	v_and_b32_e32 v65, 0xffff0000, v10
	v_max3_f32 v8, v8, |v62|, |v63|
	v_lshlrev_b32_e32 v66, 16, v11
	v_and_b32_e32 v11, 0xffff0000, v11
	v_max3_f32 v8, v8, |v64|, |v65|
	v_max3_f32 v8, v8, |v66|, |v11|
	s_waitcnt lgkmcnt(0)
	s_nop 1
	v_max_f32_dpp v9, v8, v8 quad_perm:[1,0,3,2] row_mask:0xf bank_mask:0xf
	s_nop 1
	v_max_f32_dpp v8, v9, v9 quad_perm:[2,3,0,1] row_mask:0xf bank_mask:0xf
	s_nop 1
	v_max_f32_dpp v9, v8, v8 row_half_mirror row_mask:0xf bank_mask:0xf
	s_nop 1
	v_max_f32_dpp v8, v9, v9 row_mirror row_mask:0xf bank_mask:0xf
	v_mov_b32_e32 v9, v8
	s_nop 1
	v_permlane16_swap_b32_e32 v8, v9
	v_max_f32_e32 v8, v8, v9
	v_mov_b32_e32 v9, v8
	s_nop 1
	v_permlane32_swap_b32_e32 v8, v9
	v_max_f32_e32 v8, v8, v9
	s_waitcnt lgkmcnt(0)
	v_cmp_lt_f32_e32 vcc, 0, v8
	v_mul_f32_e32 v8, 0x3c010204, v8
	s_nop 0
	v_cndmask_b32_e32 v51, 1.0, v8, vcc
	v_div_scale_f32 v8, s[12:13], v51, v51, 1.0
	v_rcp_f32_e32 v9, v8
	s_mov_b32 s12, 0x40c0c00
	v_fma_f32 v10, -v8, v9, 1.0
	v_fmac_f32_e32 v9, v10, v9
	v_div_scale_f32 v10, vcc, 1.0, v51, 1.0
	v_mul_f32_e32 v67, v10, v9
	v_fma_f32 v68, -v8, v67, v10
	v_fmac_f32_e32 v67, v68, v9
	v_fma_f32 v8, -v8, v67, v10
	v_div_fmas_f32 v8, v8, v9, v67
	v_div_fixup_f32 v67, v8, v51, 1.0
	v_mul_f32_e32 v9, v67, v52
	v_mul_f32_e32 v8, v67, v56
	v_rndne_f32_e32 v9, v9
	v_mul_f32_e32 v10, v67, v57
	v_mul_f32_e32 v52, v67, v53
	v_rndne_f32_e32 v8, v8
	v_cvt_i32_f32_e32 v9, v9
	v_rndne_f32_e32 v10, v10
	v_rndne_f32_e32 v52, v52
	v_cvt_i32_f32_e32 v8, v8
	v_cvt_i32_f32_sdwa v10, v10 dst_sel:WORD_1 dst_unused:UNUSED_PAD src0_sel:DWORD
	v_cvt_i32_f32_e32 v52, v52
	v_lshlrev_b32_e32 v9, 8, v9
	v_and_b32_e32 v9, 0xff00, v9
	v_and_b32_e32 v10, 0xff0000, v10
	v_perm_b32 v8, v52, v8, s12
	v_or3_b32 v8, v8, v9, v10
	v_mul_f32_e32 v10, v67, v54
	v_mul_f32_e32 v9, v67, v58
	v_rndne_f32_e32 v10, v10
	v_mul_f32_e32 v52, v67, v59
	v_mul_f32_e32 v53, v67, v55
	v_rndne_f32_e32 v9, v9
	v_cvt_i32_f32_e32 v10, v10
	v_rndne_f32_e32 v52, v52
	v_rndne_f32_e32 v53, v53
	v_cvt_i32_f32_e32 v9, v9
	v_cvt_i32_f32_sdwa v52, v52 dst_sel:WORD_1 dst_unused:UNUSED_PAD src0_sel:DWORD
	v_cvt_i32_f32_e32 v53, v53
	v_lshlrev_b32_e32 v10, 8, v10
	v_and_b32_e32 v10, 0xff00, v10
	v_and_b32_e32 v52, 0xff0000, v52
	v_perm_b32 v9, v53, v9, s12
	v_or3_b32 v9, v9, v10, v52
	v_mul_f32_e32 v52, v67, v61
	v_mul_f32_e32 v10, v67, v60
	v_rndne_f32_e32 v52, v52
	v_mul_f32_e32 v53, v67, v62
	v_mul_f32_e32 v54, v67, v63
	v_rndne_f32_e32 v10, v10
	v_cvt_i32_f32_e32 v52, v52
	v_rndne_f32_e32 v53, v53
	v_rndne_f32_e32 v54, v54
	v_cvt_i32_f32_e32 v10, v10
	v_cvt_i32_f32_sdwa v53, v53 dst_sel:WORD_1 dst_unused:UNUSED_PAD src0_sel:DWORD
	v_cvt_i32_f32_e32 v54, v54
	v_lshlrev_b32_e32 v52, 8, v52
	v_and_b32_e32 v52, 0xff00, v52
	v_and_b32_e32 v53, 0xff0000, v53
	v_perm_b32 v10, v54, v10, s12
	v_or3_b32 v10, v10, v52, v53
	v_mul_f32_e32 v52, v67, v64
	v_mul_f32_e32 v11, v67, v11
	v_rndne_f32_e32 v52, v52
	v_rndne_f32_e32 v11, v11
	v_cvt_i32_f32_e32 v52, v52
	v_cvt_i32_f32_e32 v11, v11
	v_cmp_eq_u32_e32 vcc, 1, v50
	v_mul_f32_e32 v53, v67, v65
	v_rndne_f32_e32 v53, v53
	v_perm_b32 v11, v11, v52, s12
	v_ffbh_u32_e32 v52, v25
	v_min_u32_e32 v52, 32, v52
	v_lshlrev_b64 v[24:25], v52, v[24:25]
	v_min_u32_e32 v24, 1, v24
	v_or_b32_e32 v24, v25, v24
	v_cvt_f32_u32_e32 v24, v24
	v_sub_u32_e32 v25, 32, v52
	v_mul_f32_e32 v54, v67, v66
	v_cvt_i32_f32_e32 v53, v53
	v_ldexp_f32 v24, v24, v25
	v_mul_f32_e32 v24, 0x33800000, v24
	v_fmamk_f32 v24, v24, 0x3a800000, v249
	v_rsq_f32_e32 v24, v24
	v_rndne_f32_e32 v54, v54
	v_cvt_i32_f32_sdwa v54, v54 dst_sel:WORD_1 dst_unused:UNUSED_PAD src0_sel:DWORD
	v_lshlrev_b32_e32 v53, 8, v53
	v_mul_f32_e32 v51, v24, v51
	v_cndmask_b32_e32 v24, 0, v26, vcc
	v_cmp_eq_u32_e32 vcc, 2, v50
	v_and_b32_e32 v53, 0xff00, v53
	v_and_b32_e32 v54, 0xff0000, v54
	v_cndmask_b32_e32 v24, v24, v28, vcc
	v_cmp_eq_u32_e32 vcc, 3, v50
	v_or3_b32 v11, v11, v53, v54
	s_nop 0
	v_cndmask_b32_e32 v24, v24, v30, vcc
	v_cmp_eq_u32_e32 vcc, 4, v50
	s_nop 1
	v_cndmask_b32_e32 v24, v24, v32, vcc
	v_cmp_eq_u32_e32 vcc, 5, v50
	s_nop 1
	v_cndmask_b32_e32 v24, v24, v34, vcc
	v_cmp_eq_u32_e32 vcc, 6, v50
	s_nop 1
	v_cndmask_b32_e32 v24, v24, v36, vcc
	v_cmp_eq_u32_e32 vcc, 7, v50
	s_nop 1
	v_cndmask_b32_e32 v24, v24, v38, vcc
	v_add_u32_e32 v24, v24, v49
	v_ashrrev_i32_e32 v25, 31, v24
	v_lshlrev_b64 v[52:53], 10, v[24:25]
	v_lshl_add_u64 v[52:53], v[14:15], 0, v[52:53]
	flat_store_dwordx4 v[52:53], v[8:11]
	s_and_saveexec_b64 s[12:13], s[4:5]
	s_cbranch_execz .LBB0_1459
	v_mov_b64_e32 v[54:55], s[10:11]
	v_lshl_add_u64 v[52:53], v[24:25], 2, s[0:1]
	flat_store_dword v[54:55], v24
	flat_store_dword v[52:53], v51

; __device__ __forceinline__ float rstd_from_fix(u64_t q) { return __builtin_amdgcn_rsqf((float)q * (1.0f / 16777216.0f) * (1.0f / D) + EPS); }
; __device__ __forceinline__ void unpack8(const u32x4& w, f32x4& a, f32x4& b) { a = (f32x4){bf_lo(w.x), bf_hi(w.x), bf_lo(w.y), bf_hi(w.y)}; b = (f32x4){bf_lo(w.z), bf_hi(w.z), bf_lo(w.w), bf_hi(w.w)}; }
; #define Q4(V) (((unsigned)(int)__builtin_rintf(V[0] * inv) & 255u) | (((unsigned)(int)__builtin_rintf(V[1] * inv) & 255u) << 8) | (((unsigned)(int)__builtin_rintf(V[2] * inv) & 255u) << 16) | (((unsigned)(int)__builtin_rintf(V[3] * inv) & 255u) << 24))
; #define Q4(V) (((unsigned)(int)__builtin_rintf(V[0] * inv) & 255u) | (((unsigned)(int)__builtin_rintf(V[1] * inv) & 255u) << 8) | (((unsigned)(int)__builtin_rintf(V[2] * inv) & 255u) << 16) | (((unsigned)(int)__builtin_rintf(V[3] * inv) & 255u) << 24))
; #define Q4(V) (((unsigned)(int)__builtin_rintf(V[0] * inv) & 255u) | (((unsigned)(int)__builtin_rintf(V[1] * inv) & 255u) << 8) | (((unsigned)(int)__builtin_rintf(V[2] * inv) & 255u) << 16) | (((unsigned)(int)__builtin_rintf(V[3] * inv) & 255u) << 24))
; __device__ __forceinline__ void phase_moe_gather(const Frame& F, bool dry) {
;     ...
;         for (int k = 0; k < 2; ++k) { const int tok = t0 + k * NGW; if (tok >= NTOK) continue;
;             f32x4 v[4]; unpack8(w0[k], v[0], v[1]); unpack8(w1[k], v[2], v[3]);
;             float am = 0.f;
; #pragma unroll
;             for (int i = 0; i < 4; ++i)
; #pragma unroll
;                 for (int j = 0; j < 4; ++j) am = fmaxf(am, fabsf(v[i][j]));
; #pragma unroll
;             for (int o = 1; o < 64; o <<= 1) am = fmaxf(am, __shfl_xor(am, o));
;             const float sc = am > 0.f ? am * (1.0f / 127.0f) : 1.0f, inv = 1.0f / sc; u32x4 q;
;     ...
;             q.x = Q4(v[0]); q.y = Q4(v[1]); q.z = Q4(v[2]); q.w = Q4(v[3]);
;     ...
;             const float rr = rstd_from_fix(sq[k]);
; #pragma unroll
;             for (int s2 = 0; s2 < 2; ++s2) { const int ee = e[2 * k + s2]; int ps = 0;
; #pragma unroll
;                 for (int j = 0; j < NE; ++j) ps = (ee == j) ? pstart[j] : ps;
;                 const int slot = ps + rk[2 * k + s2];
;                 if (!dry) { ((u32x4*)(XP8 + (size_t)slot * D))[lane] = q; if (lane == 0) { tokslot[2 * tok + s2] = slot; slotr[slot] = sc * rr; } } } }
.LBB0_1462:
	v_lshlrev_b32_e32 v8, 16, v4
	v_and_b32_e32 v4, 0xffff0000, v4
	v_lshlrev_b32_e32 v9, 16, v5
	v_and_b32_e32 v5, 0xffff0000, v5
	v_lshlrev_b32_e32 v24, 16, v0
	v_and_b32_e32 v25, 0xffff0000, v0
	v_max3_f32 v0, |v8|, 0, |v4|
	v_lshlrev_b32_e32 v10, 16, v6
	v_and_b32_e32 v6, 0xffff0000, v6
	v_max3_f32 v0, v0, |v9|, |v5|
	v_lshlrev_b32_e32 v11, 16, v7
	v_and_b32_e32 v7, 0xffff0000, v7
	v_max3_f32 v0, v0, |v10|, |v6|
	v_max3_f32 v0, v0, |v11|, |v7|
	v_lshlrev_b32_e32 v47, 16, v1
	v_and_b32_e32 v48, 0xffff0000, v1
	v_max3_f32 v0, v0, |v24|, |v25|
	v_lshlrev_b32_e32 v49, 16, v2
	v_and_b32_e32 v50, 0xffff0000, v2
	v_max3_f32 v0, v0, |v47|, |v48|
	v_lshlrev_b32_e32 v51, 16, v3
	v_and_b32_e32 v3, 0xffff0000, v3
	v_max3_f32 v0, v0, |v49|, |v50|
	v_max3_f32 v0, v0, |v51|, |v3|
	s_waitcnt lgkmcnt(0)
	s_nop 1
	v_max_f32_dpp v1, v0, v0 quad_perm:[1,0,3,2] row_mask:0xf bank_mask:0xf
	s_nop 1
	v_max_f32_dpp v0, v1, v1 quad_perm:[2,3,0,1] row_mask:0xf bank_mask:0xf
	s_nop 1
	v_max_f32_dpp v1, v0, v0 row_half_mirror row_mask:0xf bank_mask:0xf
	s_nop 1
	v_max_f32_dpp v0, v1, v1 row_mirror row_mask:0xf bank_mask:0xf
	v_mov_b32_e32 v1, v0
	s_nop 1
	v_permlane16_swap_b32_e32 v0, v1
	v_max_f32_e32 v0, v0, v1
	v_mov_b32_e32 v1, v0
	s_nop 1
	v_permlane32_swap_b32_e32 v0, v1
	v_max_f32_e32 v0, v0, v1
	s_waitcnt lgkmcnt(0)
	v_mul_f32_e32 v1, 0x3c010204, v0
	v_cmp_lt_f32_e32 vcc, 0, v0
	s_nop 1
	v_cndmask_b32_e32 v52, 1.0, v1, vcc
	v_div_scale_f32 v0, s[10:11], v52, v52, 1.0
	v_rcp_f32_e32 v1, v0
	v_div_scale_f32 v2, vcc, 1.0, v52, 1.0
	s_mov_b32 s10, 0x40c0c00
	v_fma_f32 v53, -v0, v1, 1.0
	v_fmac_f32_e32 v1, v53, v1
	v_mul_f32_e32 v53, v2, v1
	v_fma_f32 v54, -v0, v53, v2
	v_fmac_f32_e32 v53, v54, v1
	v_fma_f32 v0, -v0, v53, v2
	v_div_fmas_f32 v0, v0, v1, v53
	v_div_fixup_f32 v53, v0, v52, 1.0
	v_mul_f32_e32 v1, v53, v4
	v_mul_f32_e32 v0, v53, v8
	v_mul_f32_e32 v2, v53, v9
	v_mul_f32_e32 v4, v53, v5
	v_rndne_f32_e32 v1, v1
	v_rndne_f32_e32 v0, v0
	v_rndne_f32_e32 v2, v2
	v_rndne_f32_e32 v4, v4
	v_cvt_i32_f32_e32 v1, v1
	v_cvt_i32_f32_sdwa v2, v2 dst_sel:WORD_1 dst_unused:UNUSED_PAD src0_sel:DWORD
	v_cvt_i32_f32_e32 v0, v0
	v_cvt_i32_f32_e32 v4, v4
	v_lshlrev_b32_e32 v1, 8, v1
	v_and_b32_e32 v2, 0xff0000, v2
	v_and_b32_e32 v1, 0xff00, v1
	v_perm_b32 v0, v4, v0, s10
	v_or3_b32 v0, v0, v1, v2
	v_mul_f32_e32 v2, v53, v6
	v_mul_f32_e32 v1, v53, v10
	v_rndne_f32_e32 v2, v2
	v_mul_f32_e32 v4, v53, v11
	v_mul_f32_e32 v5, v53, v7
	v_rndne_f32_e32 v1, v1
	v_cvt_i32_f32_e32 v2, v2
	v_rndne_f32_e32 v4, v4
	v_rndne_f32_e32 v5, v5
	v_cvt_i32_f32_e32 v1, v1
	v_cvt_i32_f32_sdwa v4, v4 dst_sel:WORD_1 dst_unused:UNUSED_PAD src0_sel:DWORD
	v_cvt_i32_f32_e32 v5, v5
	v_lshlrev_b32_e32 v2, 8, v2
	v_and_b32_e32 v2, 0xff00, v2
	v_and_b32_e32 v4, 0xff0000, v4
	v_perm_b32 v1, v5, v1, s10
	v_or3_b32 v1, v1, v2, v4
	v_mul_f32_e32 v4, v53, v25
	v_mul_f32_e32 v2, v53, v24
	v_rndne_f32_e32 v4, v4
	v_mul_f32_e32 v5, v53, v47
	v_mul_f32_e32 v6, v53, v48
	v_rndne_f32_e32 v2, v2
	v_cvt_i32_f32_e32 v4, v4
	v_rndne_f32_e32 v5, v5
	v_rndne_f32_e32 v6, v6
	v_cvt_i32_f32_e32 v2, v2
	v_cvt_i32_f32_sdwa v5, v5 dst_sel:WORD_1 dst_unused:UNUSED_PAD src0_sel:DWORD
	v_cvt_i32_f32_e32 v6, v6
	v_lshlrev_b32_e32 v4, 8, v4
	v_and_b32_e32 v4, 0xff00, v4
	v_and_b32_e32 v5, 0xff0000, v5
	v_perm_b32 v2, v6, v2, s10
	v_or3_b32 v2, v2, v4, v5
	v_mul_f32_e32 v4, v53, v50
	v_rndne_f32_e32 v4, v4
	v_cvt_i32_f32_e32 v4, v4
	v_mul_f32_e32 v5, v53, v49
	v_rndne_f32_e32 v5, v5
	v_cvt_i32_f32_e32 v6, v5
	v_lshlrev_b32_e32 v4, 8, v4
	v_and_b32_e32 v7, 0xff00, v4
	v_mul_f32_e32 v4, v53, v51
	v_rndne_f32_e32 v4, v4
	v_cvt_i32_f32_sdwa v8, v4 dst_sel:WORD_1 dst_unused:UNUSED_PAD src0_sel:DWORD
	v_ffbh_u32_e32 v4, v23
	v_min_u32_e32 v9, 32, v4
	v_lshlrev_b64 v[4:5], v9, v[22:23]
	v_min_u32_e32 v4, 1, v4
	v_or_b32_e32 v4, v5, v4
	v_cvt_f32_u32_e32 v4, v4
	v_sub_u32_e32 v5, 32, v9
	v_mul_f32_e32 v3, v53, v3
	v_rndne_f32_e32 v3, v3
	v_ldexp_f32 v4, v4, v5
	v_mul_f32_e32 v4, 0x33800000, v4
	v_fmamk_f32 v4, v4, 0x3a800000, v249
	v_cvt_i32_f32_e32 v3, v3
	v_rsq_f32_e32 v4, v4
	v_cmp_eq_u32_e32 vcc, 1, v16
	v_and_b32_e32 v5, 0xff0000, v8
	v_perm_b32 v3, v3, v6, s10
	v_mul_f32_e32 v6, v4, v52
	v_cndmask_b32_e32 v4, 0, v26, vcc
	v_cmp_eq_u32_e32 vcc, 2, v16
	v_or3_b32 v3, v3, v7, v5
	s_add_i32 s10, s81, s8
	v_cndmask_b32_e32 v4, v4, v28, vcc
	v_cmp_eq_u32_e32 vcc, 3, v16
	s_nop 1
	v_cndmask_b32_e32 v4, v4, v30, vcc
	v_cmp_eq_u32_e32 vcc, 4, v16
	s_nop 1
	v_cndmask_b32_e32 v4, v4, v32, vcc
	v_cmp_eq_u32_e32 vcc, 5, v16
	s_nop 1
	v_cndmask_b32_e32 v4, v4, v34, vcc
	v_cmp_eq_u32_e32 vcc, 6, v16
	s_nop 1
	v_cndmask_b32_e32 v4, v4, v36, vcc
	v_cmp_eq_u32_e32 vcc, 7, v16
	s_nop 1
	v_cndmask_b32_e32 v4, v4, v38, vcc
	v_add_u32_e32 v4, v4, v18
	v_ashrrev_i32_e32 v5, 31, v4
	v_lshlrev_b64 v[8:9], 10, v[4:5]
	v_lshl_add_u64 v[8:9], v[14:15], 0, v[8:9]
	flat_store_dwordx4 v[8:9], v[0:3]
	s_and_saveexec_b64 s[12:13], s[4:5]
	s_cbranch_execz .LBB0_1464
	s_ashr_i32 s11, s10, 31
	s_lshl_b64 s[14:15], s[10:11], 2
	s_add_u32 s14, s36, s14
	s_addc_u32 s15, s37, s15
	v_mov_b64_e32 v[10:11], s[14:15]
	v_lshl_add_u64 v[8:9], v[4:5], 2, s[0:1]
	flat_store_dword v[10:11], v4
	flat_store_dword v[8:9], v6

; __device__ __forceinline__ float rstd_from_fix(u64_t q) { return __builtin_amdgcn_rsqf((float)q * (1.0f / 16777216.0f) * (1.0f / D) + EPS); }
; __device__ __forceinline__ void unpack8(const u32x4& w, f32x4& a, f32x4& b) { a = (f32x4){bf_lo(w.x), bf_hi(w.x), bf_lo(w.y), bf_hi(w.y)}; b = (f32x4){bf_lo(w.z), bf_hi(w.z), bf_lo(w.w), bf_hi(w.w)}; }
; #define Q4(V) (((unsigned)(int)__builtin_rintf(V[0] * inv) & 255u) | (((unsigned)(int)__builtin_rintf(V[1] * inv) & 255u) << 8) | (((unsigned)(int)__builtin_rintf(V[2] * inv) & 255u) << 16) | (((unsigned)(int)__builtin_rintf(V[3] * inv) & 255u) << 24))
; #define Q4(V) (((unsigned)(int)__builtin_rintf(V[0] * inv) & 255u) | (((unsigned)(int)__builtin_rintf(V[1] * inv) & 255u) << 8) | (((unsigned)(int)__builtin_rintf(V[2] * inv) & 255u) << 16) | (((unsigned)(int)__builtin_rintf(V[3] * inv) & 255u) << 24))
; __device__ __forceinline__ void quant_pass(const bf16_t* XB, unsigned char* XQ, float* rsq, const u64_t* ssq, int gw, int NGW, int lane, bool dry) {
;     for (int r0 = gw; r0 < NTOK; r0 += 4 * NGW) {
;         u32x4 w0[4], w1[4]; u64_t sq[4];
; #pragma unroll
;         for (int k = 0; k < 4; ++k) { const int row = r0 + k * NGW; const int rr = row < NTOK ? row : 0; w0[k] = ((const u32x4*)(XB + (size_t)rr * D))[2 * lane]; w1[k] = ((const u32x4*)(XB + (size_t)rr * D))[2 * lane + 1]; sq[k] = ssq[rr]; }
; #pragma unroll
;         for (int k = 0; k < 4; ++k) { const int row = r0 + k * NGW; if (row >= NTOK) continue;
;             f32x4 v[4]; unpack8(w0[k], v[0], v[1]); unpack8(w1[k], v[2], v[3]);
;             float am = 0.f;
; #pragma unroll
;             for (int i = 0; i < 4; ++i)
; #pragma unroll
;                 for (int j = 0; j < 4; ++j) am = fmaxf(am, fabsf(v[i][j]));
; #pragma unroll
;             for (int o = 1; o < 64; o <<= 1) am = fmaxf(am, __shfl_xor(am, o));
;             const float sc = am > 0.f ? am * (1.0f / 127.0f) : 1.0f, inv = 1.0f / sc; u32x4 q;
;     ...
;             q.x = Q4(v[0]); q.y = Q4(v[1]); q.z = Q4(v[2]); q.w = Q4(v[3]);
;     ...
;             if (!dry) { ((u32x4*)(XQ + (size_t)row * D))[lane] = q; if (lane == 0) rsq[row] = sc * rstd_from_fix(sq[k]); } }
.LBB0_1701:
	s_ashr_i32 s9, s8, 31
	s_lshl_b64 s[2:3], s[8:9], 3
	s_add_u32 s2, s12, s2
	s_addc_u32 s3, s13, s3
	v_mov_b64_e32 v[0:1], s[2:3]
	s_add_i32 s2, s8, s76
	s_cmp_lt_i32 s2, 0x8000
	s_cselect_b32 s4, s2, 0
	s_ashr_i32 s5, s4, 31
	s_lshl_b64 s[6:7], s[4:5], 11
	s_lshl_b64 s[4:5], s[4:5], 3
	s_add_u32 s4, s12, s4
	flat_load_dwordx2 v[38:39], v[0:1]
	v_lshl_add_u64 v[0:1], v[28:29], 0, s[6:7]
	s_addc_u32 s5, s13, s5
	s_add_i32 s6, s81, s8
	s_cmp_lt_i32 s6, 0x8000
	flat_load_dwordx4 v[20:23], v[0:1]
	flat_load_dwordx4 v[16:19], v[0:1] offset:16
	v_mov_b64_e32 v[0:1], s[4:5]
	s_cselect_b32 s4, s6, 0
	s_ashr_i32 s5, s4, 31
	s_lshl_b64 s[10:11], s[4:5], 11
	s_lshl_b64 s[4:5], s[4:5], 3
	s_add_u32 s4, s12, s4
	flat_load_dwordx2 v[36:37], v[0:1]
	v_lshl_add_u64 v[0:1], v[28:29], 0, s[10:11]
	s_addc_u32 s5, s13, s5
	s_mul_i32 s3, s78, 24
	flat_load_dwordx4 v[12:15], v[0:1]
	flat_load_dwordx4 v[8:11], v[0:1] offset:16
	v_mov_b64_e32 v[0:1], s[4:5]
	s_add_i32 s4, s3, s8
	s_cmp_lt_i32 s4, 0x8000
	s_cselect_b32 s10, s4, 0
	s_ashr_i32 s11, s10, 31
	s_lshl_b64 s[14:15], s[10:11], 11
	s_lshl_b64 s[10:11], s[10:11], 3
	s_add_u32 s10, s12, s10
	s_addc_u32 s11, s13, s11
	v_mov_b64_e32 v[24:25], s[10:11]
	s_lshl_b64 s[10:11], s[8:9], 11
	flat_load_dwordx2 v[34:35], v[0:1]
	v_lshl_add_u64 v[0:1], v[28:29], 0, s[14:15]
	v_lshl_add_u64 v[46:47], v[28:29], 0, s[10:11]
	flat_load_dwordx4 v[4:7], v[0:1]
	s_nop 0
	flat_load_dwordx4 v[0:3], v[0:1] offset:16
	s_mov_b32 s3, 0x40c0c00
	flat_load_dwordx2 v[32:33], v[24:25]
	s_nop 0
	flat_load_dwordx4 v[24:27], v[46:47] offset:16
	s_nop 0
	flat_load_dwordx4 v[46:49], v[46:47]
	s_waitcnt vmcnt(0) lgkmcnt(0)
	v_lshlrev_b32_e32 v55, 16, v24
	v_lshlrev_b32_e32 v50, 16, v46
	v_and_b32_e32 v51, 0xffff0000, v46
	v_lshlrev_b32_e32 v52, 16, v47
	v_and_b32_e32 v47, 0xffff0000, v47
	v_and_b32_e32 v56, 0xffff0000, v24
	v_max3_f32 v24, |v50|, 0, |v51|
	v_lshlrev_b32_e32 v53, 16, v48
	v_and_b32_e32 v48, 0xffff0000, v48
	v_max3_f32 v24, v24, |v52|, |v47|
	v_lshlrev_b32_e32 v54, 16, v49
	v_and_b32_e32 v49, 0xffff0000, v49
	v_max3_f32 v24, v24, |v53|, |v48|
	v_max3_f32 v24, v24, |v54|, |v49|
	v_lshlrev_b32_e32 v57, 16, v25
	v_and_b32_e32 v58, 0xffff0000, v25
	v_max3_f32 v24, v24, |v55|, |v56|
	v_lshlrev_b32_e32 v59, 16, v26
	v_and_b32_e32 v60, 0xffff0000, v26
	v_max3_f32 v24, v24, |v57|, |v58|
	v_lshlrev_b32_e32 v61, 16, v27
	v_and_b32_e32 v27, 0xffff0000, v27
	v_max3_f32 v24, v24, |v59|, |v60|
	v_max3_f32 v24, v24, |v61|, |v27|
	s_waitcnt lgkmcnt(0)
	s_nop 1
	v_max_f32_dpp v25, v24, v24 quad_perm:[1,0,3,2] row_mask:0xf bank_mask:0xf
	s_nop 1
	v_max_f32_dpp v24, v25, v25 quad_perm:[2,3,0,1] row_mask:0xf bank_mask:0xf
	s_nop 1
	v_max_f32_dpp v25, v24, v24 row_half_mirror row_mask:0xf bank_mask:0xf
	s_nop 1
	v_max_f32_dpp v24, v25, v25 row_mirror row_mask:0xf bank_mask:0xf
	v_mov_b32_e32 v25, v24
	s_nop 1
	v_permlane16_swap_b32_e32 v24, v25
	v_max_f32_e32 v24, v24, v25
	v_mov_b32_e32 v25, v24
	s_nop 1
	v_permlane32_swap_b32_e32 v24, v25
	v_max_f32_e32 v24, v24, v25
	s_waitcnt lgkmcnt(0)
	v_cmp_lt_f32_e32 vcc, 0, v24
	v_mul_f32_e32 v24, 0x3c010204, v24
	s_nop 0
	v_cndmask_b32_e32 v46, 1.0, v24, vcc
	v_div_scale_f32 v24, s[10:11], v46, v46, 1.0
	v_rcp_f32_e32 v25, v24
	s_lshl_b64 s[10:11], s[8:9], 10
	v_fma_f32 v26, -v24, v25, 1.0
	v_fmac_f32_e32 v25, v26, v25
	v_div_scale_f32 v26, vcc, 1.0, v46, 1.0
	v_mul_f32_e32 v62, v26, v25
	v_fma_f32 v63, -v24, v62, v26
	v_fmac_f32_e32 v62, v63, v25
	v_fma_f32 v24, -v24, v62, v26
	v_div_fmas_f32 v24, v24, v25, v62
	v_div_fixup_f32 v62, v24, v46, 1.0
	v_mul_f32_e32 v25, v62, v51
	v_mul_f32_e32 v24, v62, v50
	v_rndne_f32_e32 v25, v25
	v_mul_f32_e32 v26, v62, v52
	v_mul_f32_e32 v47, v62, v47
	v_rndne_f32_e32 v24, v24
	v_cvt_i32_f32_e32 v25, v25
	v_rndne_f32_e32 v26, v26
	v_rndne_f32_e32 v47, v47
	v_cvt_i32_f32_e32 v24, v24
	v_cvt_i32_f32_sdwa v26, v26 dst_sel:WORD_1 dst_unused:UNUSED_PAD src0_sel:DWORD
	v_cvt_i32_f32_e32 v47, v47
	v_lshlrev_b32_e32 v25, 8, v25
	v_and_b32_e32 v25, 0xff00, v25
	v_and_b32_e32 v26, 0xff0000, v26
	v_perm_b32 v24, v47, v24, s3
	v_or3_b32 v24, v24, v25, v26
	v_mul_f32_e32 v26, v62, v48
	v_mul_f32_e32 v25, v62, v53
	v_rndne_f32_e32 v26, v26
	v_mul_f32_e32 v47, v62, v54
	v_mul_f32_e32 v48, v62, v49
	v_rndne_f32_e32 v25, v25
	v_cvt_i32_f32_e32 v26, v26
	v_rndne_f32_e32 v47, v47
	v_rndne_f32_e32 v48, v48
	v_cvt_i32_f32_e32 v25, v25
	v_cvt_i32_f32_sdwa v47, v47 dst_sel:WORD_1 dst_unused:UNUSED_PAD src0_sel:DWORD
	v_cvt_i32_f32_e32 v48, v48
	v_lshlrev_b32_e32 v26, 8, v26
	v_and_b32_e32 v26, 0xff00, v26
	v_and_b32_e32 v47, 0xff0000, v47
	v_perm_b32 v25, v48, v25, s3
	v_or3_b32 v25, v25, v26, v47
	v_mul_f32_e32 v47, v62, v56
	v_mul_f32_e32 v26, v62, v55
	v_rndne_f32_e32 v47, v47
	v_mul_f32_e32 v48, v62, v57
	v_mul_f32_e32 v49, v62, v58
	v_rndne_f32_e32 v26, v26
	v_cvt_i32_f32_e32 v47, v47
	v_rndne_f32_e32 v48, v48
	v_rndne_f32_e32 v49, v49
	v_cvt_i32_f32_e32 v26, v26
	v_cvt_i32_f32_sdwa v48, v48 dst_sel:WORD_1 dst_unused:UNUSED_PAD src0_sel:DWORD
	v_cvt_i32_f32_e32 v49, v49
	v_lshlrev_b32_e32 v47, 8, v47
	v_and_b32_e32 v47, 0xff00, v47
	v_and_b32_e32 v48, 0xff0000, v48
	v_perm_b32 v26, v49, v26, s3
	v_or3_b32 v26, v26, v47, v48
	v_mul_f32_e32 v48, v62, v60
	v_mul_f32_e32 v47, v62, v59
	v_rndne_f32_e32 v48, v48
	v_mul_f32_e32 v49, v62, v61
	v_mul_f32_e32 v27, v62, v27
	v_rndne_f32_e32 v47, v47
	v_cvt_i32_f32_e32 v48, v48
	v_rndne_f32_e32 v49, v49
	v_rndne_f32_e32 v27, v27
	v_cvt_i32_f32_e32 v47, v47
	v_cvt_i32_f32_sdwa v49, v49 dst_sel:WORD_1 dst_unused:UNUSED_PAD src0_sel:DWORD
	v_cvt_i32_f32_e32 v27, v27
	v_lshlrev_b32_e32 v48, 8, v48
	v_and_b32_e32 v48, 0xff00, v48
	v_and_b32_e32 v49, 0xff0000, v49
	v_perm_b32 v27, v27, v47, s3
	v_or3_b32 v27, v27, v48, v49
	v_lshl_add_u64 v[48:49], v[30:31], 0, s[10:11]
	flat_store_dwordx4 v[48:49], v[24:27]
	s_and_saveexec_b64 s[10:11], s[0:1]
	s_cbranch_execz .LBB0_1707
	v_ffbh_u32_e32 v24, v39
	v_min_u32_e32 v26, 32, v24
	v_lshlrev_b64 v[24:25], v26, v[38:39]
	v_min_u32_e32 v24, 1, v24
	v_or_b32_e32 v24, v25, v24
	v_cvt_f32_u32_e32 v24, v24
	v_sub_u32_e32 v25, 32, v26
	s_lshl_b64 s[8:9], s[8:9], 2
	s_add_u32 s8, s30, s8
	v_ldexp_f32 v24, v24, v25
	v_mul_f32_e32 v24, 0x33800000, v24
	v_fmamk_f32 v24, v24, 0x3a800000, v249
	v_rsq_f32_e32 v24, v24
	s_addc_u32 s9, s31, s9
	v_mul_f32_e32 v26, v24, v46
	v_mov_b64_e32 v[24:25], s[8:9]
	flat_store_dword v[24:25], v26
	s_or_b64 exec, exec, s[10:11]
	s_cmpk_gt_i32 s2, 0x7fff
	s_cbranch_scc0 .LBB0_1708

; __device__ __forceinline__ float rstd_from_fix(u64_t q) { return __builtin_amdgcn_rsqf((float)q * (1.0f / 16777216.0f) * (1.0f / D) + EPS); }
; __device__ __forceinline__ void unpack8(const u32x4& w, f32x4& a, f32x4& b) { a = (f32x4){bf_lo(w.x), bf_hi(w.x), bf_lo(w.y), bf_hi(w.y)}; b = (f32x4){bf_lo(w.z), bf_hi(w.z), bf_lo(w.w), bf_hi(w.w)}; }
; #define Q4(V) (((unsigned)(int)__builtin_rintf(V[0] * inv) & 255u) | (((unsigned)(int)__builtin_rintf(V[1] * inv) & 255u) << 8) | (((unsigned)(int)__builtin_rintf(V[2] * inv) & 255u) << 16) | (((unsigned)(int)__builtin_rintf(V[3] * inv) & 255u) << 24))
; #define Q4(V) (((unsigned)(int)__builtin_rintf(V[0] * inv) & 255u) | (((unsigned)(int)__builtin_rintf(V[1] * inv) & 255u) << 8) | (((unsigned)(int)__builtin_rintf(V[2] * inv) & 255u) << 16) | (((unsigned)(int)__builtin_rintf(V[3] * inv) & 255u) << 24))
; #define Q4(V) (((unsigned)(int)__builtin_rintf(V[0] * inv) & 255u) | (((unsigned)(int)__builtin_rintf(V[1] * inv) & 255u) << 8) | (((unsigned)(int)__builtin_rintf(V[2] * inv) & 255u) << 16) | (((unsigned)(int)__builtin_rintf(V[3] * inv) & 255u) << 24))
; __device__ __forceinline__ void quant_pass(const bf16_t* XB, unsigned char* XQ, float* rsq, const u64_t* ssq, int gw, int NGW, int lane, bool dry) {
;     ...
;         for (int k = 0; k < 4; ++k) { const int row = r0 + k * NGW; if (row >= NTOK) continue;
;             f32x4 v[4]; unpack8(w0[k], v[0], v[1]); unpack8(w1[k], v[2], v[3]);
;             float am = 0.f;
; #pragma unroll
;             for (int i = 0; i < 4; ++i)
; #pragma unroll
;                 for (int j = 0; j < 4; ++j) am = fmaxf(am, fabsf(v[i][j]));
; #pragma unroll
;             for (int o = 1; o < 64; o <<= 1) am = fmaxf(am, __shfl_xor(am, o));
;             const float sc = am > 0.f ? am * (1.0f / 127.0f) : 1.0f, inv = 1.0f / sc; u32x4 q;
;     ...
;             q.x = Q4(v[0]); q.y = Q4(v[1]); q.z = Q4(v[2]); q.w = Q4(v[3]);
;     ...
;             if (!dry) { ((u32x4*)(XQ + (size_t)row * D))[lane] = q; if (lane == 0) rsq[row] = sc * rstd_from_fix(sq[k]); } }
.LBB0_1704:
	v_lshlrev_b32_e32 v16, 16, v12
	v_and_b32_e32 v12, 0xffff0000, v12
	v_lshlrev_b32_e32 v17, 16, v13
	v_and_b32_e32 v13, 0xffff0000, v13
	v_lshlrev_b32_e32 v20, 16, v8
	v_and_b32_e32 v21, 0xffff0000, v8
	v_max3_f32 v8, |v16|, 0, |v12|
	v_lshlrev_b32_e32 v18, 16, v14
	v_and_b32_e32 v14, 0xffff0000, v14
	v_max3_f32 v8, v8, |v17|, |v13|
	v_lshlrev_b32_e32 v19, 16, v15
	v_and_b32_e32 v15, 0xffff0000, v15
	v_max3_f32 v8, v8, |v18|, |v14|
	v_max3_f32 v8, v8, |v19|, |v15|
	v_lshlrev_b32_e32 v22, 16, v9
	v_and_b32_e32 v9, 0xffff0000, v9
	v_max3_f32 v8, v8, |v20|, |v21|
	v_lshlrev_b32_e32 v23, 16, v10
	v_and_b32_e32 v24, 0xffff0000, v10
	v_max3_f32 v8, v8, |v22|, |v9|
	v_lshlrev_b32_e32 v25, 16, v11
	v_and_b32_e32 v26, 0xffff0000, v11
	v_max3_f32 v8, v8, |v23|, |v24|
	v_max3_f32 v8, v8, |v25|, |v26|
	s_waitcnt lgkmcnt(0)
	s_mov_b32 s3, 0x40c0c00
	s_ashr_i32 s7, s6, 31
	s_nop 1
	v_max_f32_dpp v10, v8, v8 quad_perm:[1,0,3,2] row_mask:0xf bank_mask:0xf
	s_nop 1
	v_max_f32_dpp v8, v10, v10 quad_perm:[2,3,0,1] row_mask:0xf bank_mask:0xf
	s_nop 1
	v_max_f32_dpp v10, v8, v8 row_half_mirror row_mask:0xf bank_mask:0xf
	s_nop 1
	v_max_f32_dpp v8, v10, v10 row_mirror row_mask:0xf bank_mask:0xf
	v_mov_b32_e32 v10, v8
	s_nop 1
	v_permlane16_swap_b32_e32 v8, v10
	v_max_f32_e32 v8, v8, v10
	v_mov_b32_e32 v10, v8
	s_nop 1
	v_permlane32_swap_b32_e32 v8, v10
	v_max_f32_e32 v8, v8, v10
	s_waitcnt lgkmcnt(0)
	v_mul_f32_e32 v10, 0x3c010204, v8
	v_cmp_lt_f32_e32 vcc, 0, v8
	s_nop 1
	v_cndmask_b32_e32 v8, 1.0, v10, vcc
	v_div_scale_f32 v10, s[8:9], v8, v8, 1.0
	v_rcp_f32_e32 v11, v10
	v_div_scale_f32 v27, vcc, 1.0, v8, 1.0
	s_lshl_b64 s[8:9], s[6:7], 10
	v_fma_f32 v36, -v10, v11, 1.0
	v_fmac_f32_e32 v11, v36, v11
	v_mul_f32_e32 v36, v27, v11
	v_fma_f32 v37, -v10, v36, v27
	v_fmac_f32_e32 v36, v37, v11
	v_fma_f32 v10, -v10, v36, v27
	v_div_fmas_f32 v10, v10, v11, v36
	v_div_fixup_f32 v27, v10, v8, 1.0
	v_mul_f32_e32 v11, v27, v12
	v_mul_f32_e32 v10, v27, v16
	v_mul_f32_e32 v12, v27, v17
	v_mul_f32_e32 v13, v27, v13
	v_rndne_f32_e32 v11, v11
	v_rndne_f32_e32 v10, v10
	v_rndne_f32_e32 v12, v12
	v_rndne_f32_e32 v13, v13
	v_cvt_i32_f32_e32 v11, v11
	v_cvt_i32_f32_sdwa v12, v12 dst_sel:WORD_1 dst_unused:UNUSED_PAD src0_sel:DWORD
	v_cvt_i32_f32_e32 v10, v10
	v_cvt_i32_f32_e32 v13, v13
	v_lshlrev_b32_e32 v11, 8, v11
	v_and_b32_e32 v12, 0xff0000, v12
	v_and_b32_e32 v11, 0xff00, v11
	v_perm_b32 v10, v13, v10, s3
	v_or3_b32 v10, v10, v11, v12
	v_mul_f32_e32 v12, v27, v14
	v_mul_f32_e32 v11, v27, v18
	v_rndne_f32_e32 v12, v12
	v_mul_f32_e32 v13, v27, v19
	v_mul_f32_e32 v14, v27, v15
	v_rndne_f32_e32 v11, v11
	v_cvt_i32_f32_e32 v12, v12
	v_rndne_f32_e32 v13, v13
	v_rndne_f32_e32 v14, v14
	v_cvt_i32_f32_e32 v11, v11
	v_cvt_i32_f32_sdwa v13, v13 dst_sel:WORD_1 dst_unused:UNUSED_PAD src0_sel:DWORD
	v_cvt_i32_f32_e32 v14, v14
	v_lshlrev_b32_e32 v12, 8, v12
	v_and_b32_e32 v12, 0xff00, v12
	v_and_b32_e32 v13, 0xff0000, v13
	v_perm_b32 v11, v14, v11, s3
	v_or3_b32 v11, v11, v12, v13
	v_mul_f32_e32 v13, v27, v21
	v_mul_f32_e32 v12, v27, v20
	v_rndne_f32_e32 v13, v13
	v_mul_f32_e32 v14, v27, v22
	v_mul_f32_e32 v9, v27, v9
	v_rndne_f32_e32 v12, v12
	v_cvt_i32_f32_e32 v13, v13
	v_rndne_f32_e32 v14, v14
	v_rndne_f32_e32 v9, v9
	v_cvt_i32_f32_e32 v12, v12
	v_cvt_i32_f32_sdwa v14, v14 dst_sel:WORD_1 dst_unused:UNUSED_PAD src0_sel:DWORD
	v_cvt_i32_f32_e32 v9, v9
	v_lshlrev_b32_e32 v13, 8, v13
	v_and_b32_e32 v13, 0xff00, v13
	v_and_b32_e32 v14, 0xff0000, v14
	v_perm_b32 v9, v9, v12, s3
	v_or3_b32 v12, v9, v13, v14
	v_mul_f32_e32 v13, v27, v24
	v_mul_f32_e32 v9, v27, v23
	v_rndne_f32_e32 v13, v13
	v_mul_f32_e32 v14, v27, v25
	v_mul_f32_e32 v15, v27, v26
	v_rndne_f32_e32 v9, v9
	v_cvt_i32_f32_e32 v13, v13
	v_rndne_f32_e32 v14, v14
	v_rndne_f32_e32 v15, v15
	v_cvt_i32_f32_e32 v9, v9
	v_cvt_i32_f32_sdwa v14, v14 dst_sel:WORD_1 dst_unused:UNUSED_PAD src0_sel:DWORD
	v_cvt_i32_f32_e32 v15, v15
	v_lshlrev_b32_e32 v13, 8, v13
	v_and_b32_e32 v13, 0xff00, v13
	v_and_b32_e32 v14, 0xff0000, v14
	v_perm_b32 v9, v15, v9, s3
	v_or3_b32 v13, v9, v13, v14
	v_lshl_add_u64 v[14:15], v[30:31], 0, s[8:9]
	flat_store_dwordx4 v[14:15], v[10:13]
	s_and_saveexec_b64 s[8:9], s[0:1]
	s_cbranch_execz .LBB0_1706
	v_ffbh_u32_e32 v9, v35
	v_min_u32_e32 v9, 32, v9
	v_lshlrev_b64 v[10:11], v9, v[34:35]
	v_min_u32_e32 v10, 1, v10
	v_or_b32_e32 v10, v11, v10
	v_cvt_f32_u32_e32 v10, v10
	v_sub_u32_e32 v9, 32, v9
	s_lshl_b64 s[6:7], s[6:7], 2
	s_add_u32 s6, s30, s6
	v_ldexp_f32 v9, v10, v9
	v_mul_f32_e32 v9, 0x33800000, v9
	v_fmamk_f32 v9, v9, 0x3a800000, v249
	v_rsq_f32_e32 v9, v9
	s_addc_u32 s7, s31, s7
	v_mul_f32_e32 v10, v9, v8
	v_mov_b64_e32 v[8:9], s[6:7]
	flat_store_dword v[8:9], v10

; __device__ __forceinline__ float rstd_from_fix(u64_t q) { return __builtin_amdgcn_rsqf((float)q * (1.0f / 16777216.0f) * (1.0f / D) + EPS); }
; __device__ __forceinline__ void unpack8(const u32x4& w, f32x4& a, f32x4& b) { a = (f32x4){bf_lo(w.x), bf_hi(w.x), bf_lo(w.y), bf_hi(w.y)}; b = (f32x4){bf_lo(w.z), bf_hi(w.z), bf_lo(w.w), bf_hi(w.w)}; }
; #define Q4(V) (((unsigned)(int)__builtin_rintf(V[0] * inv) & 255u) | (((unsigned)(int)__builtin_rintf(V[1] * inv) & 255u) << 8) | (((unsigned)(int)__builtin_rintf(V[2] * inv) & 255u) << 16) | (((unsigned)(int)__builtin_rintf(V[3] * inv) & 255u) << 24))
; #define Q4(V) (((unsigned)(int)__builtin_rintf(V[0] * inv) & 255u) | (((unsigned)(int)__builtin_rintf(V[1] * inv) & 255u) << 8) | (((unsigned)(int)__builtin_rintf(V[2] * inv) & 255u) << 16) | (((unsigned)(int)__builtin_rintf(V[3] * inv) & 255u) << 24))
; #define Q4(V) (((unsigned)(int)__builtin_rintf(V[0] * inv) & 255u) | (((unsigned)(int)__builtin_rintf(V[1] * inv) & 255u) << 8) | (((unsigned)(int)__builtin_rintf(V[2] * inv) & 255u) << 16) | (((unsigned)(int)__builtin_rintf(V[3] * inv) & 255u) << 24))
; __device__ __forceinline__ void quant_pass(const bf16_t* XB, unsigned char* XQ, float* rsq, const u64_t* ssq, int gw, int NGW, int lane, bool dry) {
;     ...
;         for (int k = 0; k < 4; ++k) { const int row = r0 + k * NGW; if (row >= NTOK) continue;
;             f32x4 v[4]; unpack8(w0[k], v[0], v[1]); unpack8(w1[k], v[2], v[3]);
;             float am = 0.f;
; #pragma unroll
;             for (int i = 0; i < 4; ++i)
; #pragma unroll
;                 for (int j = 0; j < 4; ++j) am = fmaxf(am, fabsf(v[i][j]));
; #pragma unroll
;             for (int o = 1; o < 64; o <<= 1) am = fmaxf(am, __shfl_xor(am, o));
;             const float sc = am > 0.f ? am * (1.0f / 127.0f) : 1.0f, inv = 1.0f / sc; u32x4 q;
;     ...
;             q.x = Q4(v[0]); q.y = Q4(v[1]); q.z = Q4(v[2]); q.w = Q4(v[3]);
;     ...
;             if (!dry) { ((u32x4*)(XQ + (size_t)row * D))[lane] = q; if (lane == 0) rsq[row] = sc * rstd_from_fix(sq[k]); } }
.LBB0_1708:
	v_lshlrev_b32_e32 v24, 16, v20
	v_and_b32_e32 v20, 0xffff0000, v20
	v_lshlrev_b32_e32 v25, 16, v21
	v_and_b32_e32 v21, 0xffff0000, v21
	v_lshlrev_b32_e32 v38, 16, v16
	v_and_b32_e32 v39, 0xffff0000, v16
	v_max3_f32 v16, |v24|, 0, |v20|
	v_lshlrev_b32_e32 v26, 16, v22
	v_and_b32_e32 v22, 0xffff0000, v22
	v_max3_f32 v16, v16, |v25|, |v21|
	v_lshlrev_b32_e32 v27, 16, v23
	v_and_b32_e32 v23, 0xffff0000, v23
	v_max3_f32 v16, v16, |v26|, |v22|
	v_max3_f32 v16, v16, |v27|, |v23|
	v_lshlrev_b32_e32 v46, 16, v17
	v_and_b32_e32 v17, 0xffff0000, v17
	v_max3_f32 v16, v16, |v38|, |v39|
	v_lshlrev_b32_e32 v47, 16, v18
	v_and_b32_e32 v48, 0xffff0000, v18
	v_max3_f32 v16, v16, |v46|, |v17|
	v_lshlrev_b32_e32 v49, 16, v19
	v_and_b32_e32 v50, 0xffff0000, v19
	v_max3_f32 v16, v16, |v47|, |v48|
	v_max3_f32 v16, v16, |v49|, |v50|
	s_waitcnt lgkmcnt(0)
	s_nop 1
	v_max_f32_dpp v18, v16, v16 quad_perm:[1,0,3,2] row_mask:0xf bank_mask:0xf
	s_nop 1
	v_max_f32_dpp v16, v18, v18 quad_perm:[2,3,0,1] row_mask:0xf bank_mask:0xf
	s_nop 1
	v_max_f32_dpp v18, v16, v16 row_half_mirror row_mask:0xf bank_mask:0xf
	s_nop 1
	v_max_f32_dpp v16, v18, v18 row_mirror row_mask:0xf bank_mask:0xf
	v_mov_b32_e32 v18, v16
	s_nop 1
	v_permlane16_swap_b32_e32 v16, v18
	v_max_f32_e32 v16, v16, v18
	v_mov_b32_e32 v18, v16
	s_nop 1
	v_permlane32_swap_b32_e32 v16, v18
	v_max_f32_e32 v16, v16, v18
	s_waitcnt lgkmcnt(0)
	v_mul_f32_e32 v18, 0x3c010204, v16
	v_cmp_lt_f32_e32 vcc, 0, v16
	s_nop 1
	v_cndmask_b32_e32 v16, 1.0, v18, vcc
	v_div_scale_f32 v18, s[8:9], v16, v16, 1.0
	v_rcp_f32_e32 v19, v18
	v_div_scale_f32 v51, vcc, 1.0, v16, 1.0
	v_fma_f32 v52, -v18, v19, 1.0
	v_fmac_f32_e32 v19, v52, v19
	v_mul_f32_e32 v52, v51, v19
	v_fma_f32 v53, -v18, v52, v51
	v_fmac_f32_e32 v52, v53, v19
	v_fma_f32 v18, -v18, v52, v51
	v_div_fmas_f32 v18, v18, v19, v52
	v_div_fixup_f32 v51, v18, v16, 1.0
	v_mul_f32_e32 v19, v51, v20
	v_mul_f32_e32 v18, v51, v24
	v_mul_f32_e32 v20, v51, v25
	v_mul_f32_e32 v21, v51, v21
	v_rndne_f32_e32 v19, v19
	v_rndne_f32_e32 v18, v18
	v_rndne_f32_e32 v20, v20
	v_rndne_f32_e32 v21, v21
	v_cvt_i32_f32_e32 v19, v19
	v_cvt_i32_f32_sdwa v20, v20 dst_sel:WORD_1 dst_unused:UNUSED_PAD src0_sel:DWORD
	v_cvt_i32_f32_e32 v18, v18
	v_cvt_i32_f32_e32 v21, v21
	v_lshlrev_b32_e32 v19, 8, v19
	v_and_b32_e32 v20, 0xff0000, v20
	v_and_b32_e32 v19, 0xff00, v19
	v_perm_b32 v18, v21, v18, s3
	v_or3_b32 v18, v18, v19, v20
	v_mul_f32_e32 v20, v51, v22
	v_mul_f32_e32 v19, v51, v26
	v_rndne_f32_e32 v20, v20
	v_mul_f32_e32 v21, v51, v27
	v_mul_f32_e32 v22, v51, v23
	v_rndne_f32_e32 v19, v19
	v_cvt_i32_f32_e32 v20, v20
	v_rndne_f32_e32 v21, v21
	v_rndne_f32_e32 v22, v22
	v_cvt_i32_f32_e32 v19, v19
	v_cvt_i32_f32_sdwa v21, v21 dst_sel:WORD_1 dst_unused:UNUSED_PAD src0_sel:DWORD
	v_cvt_i32_f32_e32 v22, v22
	v_lshlrev_b32_e32 v20, 8, v20
	v_and_b32_e32 v20, 0xff00, v20
	v_and_b32_e32 v21, 0xff0000, v21
	v_perm_b32 v19, v22, v19, s3
	v_or3_b32 v19, v19, v20, v21
	v_mul_f32_e32 v21, v51, v39
	v_mul_f32_e32 v20, v51, v38
	v_rndne_f32_e32 v21, v21
	v_mul_f32_e32 v22, v51, v46
	v_mul_f32_e32 v17, v51, v17
	v_rndne_f32_e32 v20, v20
	v_cvt_i32_f32_e32 v21, v21
	v_rndne_f32_e32 v22, v22
	v_rndne_f32_e32 v17, v17
	v_cvt_i32_f32_e32 v20, v20
	v_cvt_i32_f32_sdwa v22, v22 dst_sel:WORD_1 dst_unused:UNUSED_PAD src0_sel:DWORD
	v_cvt_i32_f32_e32 v17, v17
	v_lshlrev_b32_e32 v21, 8, v21
	v_and_b32_e32 v21, 0xff00, v21
	v_and_b32_e32 v22, 0xff0000, v22
	v_perm_b32 v17, v17, v20, s3
	v_or3_b32 v20, v17, v21, v22
	v_mul_f32_e32 v17, v51, v47
	v_mul_f32_e32 v21, v51, v48
	v_mul_f32_e32 v23, v51, v50
	v_rndne_f32_e32 v17, v17
	v_rndne_f32_e32 v21, v21
	v_mul_f32_e32 v22, v51, v49
	v_rndne_f32_e32 v23, v23
	v_cvt_i32_f32_e32 v17, v17
	v_cvt_i32_f32_e32 v21, v21
	v_rndne_f32_e32 v22, v22
	v_cvt_i32_f32_e32 v23, v23
	v_cvt_i32_f32_sdwa v22, v22 dst_sel:WORD_1 dst_unused:UNUSED_PAD src0_sel:DWORD
	v_lshlrev_b32_e32 v21, 8, v21
	v_and_b32_e32 v21, 0xff00, v21
	v_perm_b32 v17, v23, v17, s3
	s_ashr_i32 s3, s2, 31
	v_and_b32_e32 v22, 0xff0000, v22
	s_lshl_b64 s[8:9], s[2:3], 10
	v_or3_b32 v21, v17, v21, v22
	v_lshl_add_u64 v[22:23], v[30:31], 0, s[8:9]
	flat_store_dwordx4 v[22:23], v[18:21]
	s_and_saveexec_b64 s[8:9], s[0:1]
	s_cbranch_execz .LBB0_1710
	v_ffbh_u32_e32 v17, v37
	v_min_u32_e32 v17, 32, v17
	v_lshlrev_b64 v[18:19], v17, v[36:37]
	v_min_u32_e32 v18, 1, v18
	v_or_b32_e32 v18, v19, v18
	v_cvt_f32_u32_e32 v18, v18
	v_sub_u32_e32 v17, 32, v17
	s_lshl_b64 s[10:11], s[2:3], 2
	s_add_u32 s10, s30, s10
	v_ldexp_f32 v17, v18, v17
	v_mul_f32_e32 v17, 0x33800000, v17
	v_fmamk_f32 v17, v17, 0x3a800000, v249
	v_rsq_f32_e32 v17, v17
	s_addc_u32 s11, s31, s11
	v_mul_f32_e32 v18, v17, v16
	v_mov_b64_e32 v[16:17], s[10:11]
	flat_store_dword v[16:17], v18

; __device__ __forceinline__ float rstd_from_fix(u64_t q) { return __builtin_amdgcn_rsqf((float)q * (1.0f / 16777216.0f) * (1.0f / D) + EPS); }
; __device__ __forceinline__ void unpack8(const u32x4& w, f32x4& a, f32x4& b) { a = (f32x4){bf_lo(w.x), bf_hi(w.x), bf_lo(w.y), bf_hi(w.y)}; b = (f32x4){bf_lo(w.z), bf_hi(w.z), bf_lo(w.w), bf_hi(w.w)}; }
; #define Q4(V) (((unsigned)(int)__builtin_rintf(V[0] * inv) & 255u) | (((unsigned)(int)__builtin_rintf(V[1] * inv) & 255u) << 8) | (((unsigned)(int)__builtin_rintf(V[2] * inv) & 255u) << 16) | (((unsigned)(int)__builtin_rintf(V[3] * inv) & 255u) << 24))
; #define Q4(V) (((unsigned)(int)__builtin_rintf(V[0] * inv) & 255u) | (((unsigned)(int)__builtin_rintf(V[1] * inv) & 255u) << 8) | (((unsigned)(int)__builtin_rintf(V[2] * inv) & 255u) << 16) | (((unsigned)(int)__builtin_rintf(V[3] * inv) & 255u) << 24))
; #define Q4(V) (((unsigned)(int)__builtin_rintf(V[0] * inv) & 255u) | (((unsigned)(int)__builtin_rintf(V[1] * inv) & 255u) << 8) | (((unsigned)(int)__builtin_rintf(V[2] * inv) & 255u) << 16) | (((unsigned)(int)__builtin_rintf(V[3] * inv) & 255u) << 24))
; __device__ __forceinline__ void quant_pass(const bf16_t* XB, unsigned char* XQ, float* rsq, const u64_t* ssq, int gw, int NGW, int lane, bool dry) {
;     ...
;         for (int k = 0; k < 4; ++k) { const int row = r0 + k * NGW; if (row >= NTOK) continue;
;             f32x4 v[4]; unpack8(w0[k], v[0], v[1]); unpack8(w1[k], v[2], v[3]);
;             float am = 0.f;
; #pragma unroll
;             for (int i = 0; i < 4; ++i)
; #pragma unroll
;                 for (int j = 0; j < 4; ++j) am = fmaxf(am, fabsf(v[i][j]));
; #pragma unroll
;             for (int o = 1; o < 64; o <<= 1) am = fmaxf(am, __shfl_xor(am, o));
;             const float sc = am > 0.f ? am * (1.0f / 127.0f) : 1.0f, inv = 1.0f / sc; u32x4 q;
;     ...
;             q.x = Q4(v[0]); q.y = Q4(v[1]); q.z = Q4(v[2]); q.w = Q4(v[3]);
;     ...
;             if (!dry) { ((u32x4*)(XQ + (size_t)row * D))[lane] = q; if (lane == 0) rsq[row] = sc * rstd_from_fix(sq[k]); } }
.LBB0_1712:
	v_lshlrev_b32_e32 v8, 16, v4
	v_and_b32_e32 v4, 0xffff0000, v4
	v_lshlrev_b32_e32 v9, 16, v5
	v_and_b32_e32 v5, 0xffff0000, v5
	v_lshlrev_b32_e32 v12, 16, v0
	v_and_b32_e32 v13, 0xffff0000, v0
	v_max3_f32 v0, |v8|, 0, |v4|
	v_lshlrev_b32_e32 v10, 16, v6
	v_and_b32_e32 v6, 0xffff0000, v6
	v_max3_f32 v0, v0, |v9|, |v5|
	v_lshlrev_b32_e32 v11, 16, v7
	v_and_b32_e32 v7, 0xffff0000, v7
	v_max3_f32 v0, v0, |v10|, |v6|
	v_max3_f32 v0, v0, |v11|, |v7|
	v_lshlrev_b32_e32 v14, 16, v1
	v_and_b32_e32 v1, 0xffff0000, v1
	v_max3_f32 v0, v0, |v12|, |v13|
	v_lshlrev_b32_e32 v15, 16, v2
	v_and_b32_e32 v16, 0xffff0000, v2
	v_max3_f32 v0, v0, |v14|, |v1|
	v_lshlrev_b32_e32 v17, 16, v3
	v_and_b32_e32 v18, 0xffff0000, v3
	v_max3_f32 v0, v0, |v15|, |v16|
	v_max3_f32 v0, v0, |v17|, |v18|
	s_waitcnt lgkmcnt(0)
	s_mov_b32 s3, 0x40c0c00
	s_ashr_i32 s5, s4, 31
	s_nop 1
	v_max_f32_dpp v2, v0, v0 quad_perm:[1,0,3,2] row_mask:0xf bank_mask:0xf
	s_nop 1
	v_max_f32_dpp v0, v2, v2 quad_perm:[2,3,0,1] row_mask:0xf bank_mask:0xf
	s_nop 1
	v_max_f32_dpp v2, v0, v0 row_half_mirror row_mask:0xf bank_mask:0xf
	s_nop 1
	v_max_f32_dpp v0, v2, v2 row_mirror row_mask:0xf bank_mask:0xf
	v_mov_b32_e32 v2, v0
	s_nop 1
	v_permlane16_swap_b32_e32 v0, v2
	v_max_f32_e32 v0, v0, v2
	v_mov_b32_e32 v2, v0
	s_nop 1
	v_permlane32_swap_b32_e32 v0, v2
	v_max_f32_e32 v0, v0, v2
	s_waitcnt lgkmcnt(0)
	v_mul_f32_e32 v2, 0x3c010204, v0
	v_cmp_lt_f32_e32 vcc, 0, v0
	s_nop 1
	v_cndmask_b32_e32 v0, 1.0, v2, vcc
	v_div_scale_f32 v2, s[6:7], v0, v0, 1.0
	v_rcp_f32_e32 v3, v2
	v_div_scale_f32 v19, vcc, 1.0, v0, 1.0
	s_lshl_b64 s[6:7], s[4:5], 10
	v_fma_f32 v20, -v2, v3, 1.0
	v_fmac_f32_e32 v3, v20, v3
	v_mul_f32_e32 v20, v19, v3
	v_fma_f32 v21, -v2, v20, v19
	v_fmac_f32_e32 v20, v21, v3
	v_fma_f32 v2, -v2, v20, v19
	v_div_fmas_f32 v2, v2, v3, v20
	v_div_fixup_f32 v19, v2, v0, 1.0
	v_mul_f32_e32 v3, v19, v4
	v_mul_f32_e32 v2, v19, v8
	v_mul_f32_e32 v4, v19, v9
	v_mul_f32_e32 v5, v19, v5
	v_rndne_f32_e32 v3, v3
	v_rndne_f32_e32 v2, v2
	v_rndne_f32_e32 v4, v4
	v_rndne_f32_e32 v5, v5
	v_cvt_i32_f32_e32 v3, v3
	v_cvt_i32_f32_sdwa v4, v4 dst_sel:WORD_1 dst_unused:UNUSED_PAD src0_sel:DWORD
	v_cvt_i32_f32_e32 v2, v2
	v_cvt_i32_f32_e32 v5, v5
	v_lshlrev_b32_e32 v3, 8, v3
	v_and_b32_e32 v4, 0xff0000, v4
	v_and_b32_e32 v3, 0xff00, v3
	v_perm_b32 v2, v5, v2, s3
	v_or3_b32 v2, v2, v3, v4
	v_mul_f32_e32 v4, v19, v6
	v_mul_f32_e32 v3, v19, v10
	v_rndne_f32_e32 v4, v4
	v_mul_f32_e32 v5, v19, v11
	v_mul_f32_e32 v6, v19, v7
	v_rndne_f32_e32 v3, v3
	v_cvt_i32_f32_e32 v4, v4
	v_rndne_f32_e32 v5, v5
	v_rndne_f32_e32 v6, v6
	v_cvt_i32_f32_e32 v3, v3
	v_cvt_i32_f32_sdwa v5, v5 dst_sel:WORD_1 dst_unused:UNUSED_PAD src0_sel:DWORD
	v_cvt_i32_f32_e32 v6, v6
	v_lshlrev_b32_e32 v4, 8, v4
	v_and_b32_e32 v4, 0xff00, v4
	v_and_b32_e32 v5, 0xff0000, v5
	v_perm_b32 v3, v6, v3, s3
	v_or3_b32 v3, v3, v4, v5
	v_mul_f32_e32 v5, v19, v13
	v_mul_f32_e32 v4, v19, v12
	v_rndne_f32_e32 v5, v5
	v_mul_f32_e32 v6, v19, v14
	v_mul_f32_e32 v1, v19, v1
	v_rndne_f32_e32 v4, v4
	v_cvt_i32_f32_e32 v5, v5
	v_rndne_f32_e32 v6, v6
	v_rndne_f32_e32 v1, v1
	v_cvt_i32_f32_e32 v4, v4
	v_cvt_i32_f32_sdwa v6, v6 dst_sel:WORD_1 dst_unused:UNUSED_PAD src0_sel:DWORD
	v_cvt_i32_f32_e32 v1, v1
	v_lshlrev_b32_e32 v5, 8, v5
	v_and_b32_e32 v5, 0xff00, v5
	v_and_b32_e32 v6, 0xff0000, v6
	v_perm_b32 v1, v1, v4, s3
	v_or3_b32 v4, v1, v5, v6
	v_mul_f32_e32 v5, v19, v16
	v_mul_f32_e32 v1, v19, v15
	v_rndne_f32_e32 v5, v5
	v_mul_f32_e32 v6, v19, v17
	v_mul_f32_e32 v7, v19, v18
	v_rndne_f32_e32 v1, v1
	v_cvt_i32_f32_e32 v5, v5
	v_rndne_f32_e32 v6, v6
	v_rndne_f32_e32 v7, v7
	v_cvt_i32_f32_e32 v1, v1
	v_cvt_i32_f32_sdwa v6, v6 dst_sel:WORD_1 dst_unused:UNUSED_PAD src0_sel:DWORD
	v_cvt_i32_f32_e32 v7, v7
	v_lshlrev_b32_e32 v5, 8, v5
	v_and_b32_e32 v5, 0xff00, v5
	v_and_b32_e32 v6, 0xff0000, v6
	v_perm_b32 v1, v7, v1, s3
	v_or3_b32 v5, v1, v5, v6
	v_lshl_add_u64 v[6:7], v[30:31], 0, s[6:7]
	flat_store_dwordx4 v[6:7], v[2:5]
	s_and_saveexec_b64 s[6:7], s[0:1]
	s_cbranch_execz .LBB0_1699
	v_ffbh_u32_e32 v1, v33
	v_min_u32_e32 v1, 32, v1
	v_lshlrev_b64 v[2:3], v1, v[32:33]
	v_min_u32_e32 v2, 1, v2
	v_or_b32_e32 v2, v3, v2
	v_cvt_f32_u32_e32 v2, v2
	v_sub_u32_e32 v1, 32, v1
	s_lshl_b64 s[4:5], s[4:5], 2
	s_add_u32 s4, s30, s4
	v_ldexp_f32 v1, v2, v1
	v_mul_f32_e32 v1, 0x33800000, v1
	v_fmamk_f32 v1, v1, 0x3a800000, v249
	v_rsq_f32_e32 v1, v1
	s_addc_u32 s5, s31, s5
	v_mul_f32_e32 v2, v1, v0
	v_mov_b64_e32 v[0:1], s[4:5]
	flat_store_dword v[0:1], v2
	s_branch .LBB0_1699
